# m19 + the required 2 wait states between v_readlane (SGPR write) and the VALU reading that SGPR in the hand-written gates/silu epilogue heads (3 sites); no functional change
# speedup vs baseline: 1.0030x; 1.0030x over previous
; DI float sigmoid64_(float x64) { return __builtin_amdgcn_rcpf(1.0f + __builtin_amdgcn_exp2f(x64 * (-LOG2E * W8_INV))); }
;     DI void operator()(const f32x4 (&acc)[2][2][4][2], const Unit& u, int wr, int wc, int fr, int fq) const {
;     ...
;             else {
; #pragma unroll
;                 for (int ai = 0; ai < 2; ++ai)
; #pragma unroll
;                     for (int m = 0; m < 4; ++m) { unsigned char* rowp = (unsigned char*)gt + (size_t)(row0 + ai * 128 + m * 16) * 2048 + (pn - 30) * 256 + wc * 32 + 8 * fq;
;                         u32x2 o[2];
; #pragma unroll
;                         for (int bj = 0; bj < 2; ++bj) {
; #pragma unroll
;                             for (int n = 0; n < 2; ++n) { const f32x4 v = acc[ai][bj][m][n];
;                                 o[bj][n] = (unsigned)(sigmoid64_(v[0]) * 255.0f + 0.5f) | ((unsigned)(sigmoid64_(v[1]) * 255.0f + 0.5f) << 8) | ((unsigned)(sigmoid64_(v[2]) * 255.0f + 0.5f) << 16) | ((unsigned)(sigmoid64_(v[3]) * 255.0f + 0.5f) << 24); } }
;                         st_pair16(rowp, 128, o[0], o[1], fq); }
;                 return; }
.LBB0_283:
	s_lshl_b32 s4, s16, 8
	s_add_i32 s4, s4, s87
	v_add_u32_e32 v10, s4, v6
	s_add_i32 s4, s43, -12
	s_cmp_gt_u32 s4, 11
	s_mov_b64 s[16:17], -1
	s_cbranch_scc0 .LBB0_299
	s_cmp_lg_u32 s43, 38
	s_cbranch_scc0 .LBB0_310
	s_cmp_gt_i32 s43, 1
	s_cbranch_scc0 .LBB0_301
	s_cmp_gt_u32 s43, 3
	s_cbranch_scc0 .LBB0_302
	s_cmp_gt_u32 s43, 7
	s_cbranch_scc0 .LBB0_297
	s_cmp_gt_u32 s43, 11
	s_cbranch_scc0 .LBB0_294
	s_cmp_lt_u32 s43, 30
	s_cbranch_scc1 .LBB0_291
	s_lshl_b32 s4, s43, 8
	s_addk_i32 s4, 0xe200
	s_ashr_i32 s5, s4, 31
	v_bfe_i32 v6, v18, 0, 1
	v_and_b32_e32 v14, 0x78, v6
	v_mov_b32_e32 v15, v4
	v_ashrrev_i32_e32 v11, 31, v10
	v_lshlrev_b64 v[6:7], 11, v[10:11]
	v_readlane_b32 s6, v255, 24
	v_readlane_b32 s7, v255, 25
	s_nop 1
	v_lshl_add_u64 v[6:7], s[6:7], 0, v[6:7]
	v_lshl_add_u64 v[6:7], v[6:7], 0, s[4:5]
	v_readlane_b32 s4, v255, 36
	v_readlane_b32 s5, v255, 37
	s_nop 1
	v_lshl_add_u64 v[16:17], v[6:7], 0, s[4:5]
	v_lshlrev_b32_e32 v12, 3, v18
	v_ashrrev_i32_e32 v13, 31, v12
	v_lshl_add_u64 v[12:13], v[16:17], 0, v[12:13]
	v_lshl_add_u64 v[12:13], v[12:13], 0, v[14:15]
	s_mov_b32 s6, 0x437f0000
	s_mov_b32 s4, 0xbcb8aa3b
	s_mov_b64 s[16:17], 0
	v_pk_mul_f32 v[150:151], v[150:151], s[4:5] op_sel_hi:[1,0]
	v_pk_mul_f32 v[152:153], v[152:153], s[4:5] op_sel_hi:[1,0]
	v_pk_mul_f32 v[154:155], v[154:155], s[4:5] op_sel_hi:[1,0]
	v_pk_mul_f32 v[156:157], v[156:157], s[4:5] op_sel_hi:[1,0]
	v_pk_mul_f32 v[158:159], v[158:159], s[4:5] op_sel_hi:[1,0]
	v_pk_mul_f32 v[160:161], v[160:161], s[4:5] op_sel_hi:[1,0]
	v_pk_mul_f32 v[162:163], v[162:163], s[4:5] op_sel_hi:[1,0]
	v_pk_mul_f32 v[164:165], v[164:165], s[4:5] op_sel_hi:[1,0]
	v_exp_f32_e32 v150, v150
	v_exp_f32_e32 v151, v151
	v_exp_f32_e32 v152, v152
	v_exp_f32_e32 v153, v153
	v_exp_f32_e32 v154, v154
	v_exp_f32_e32 v155, v155
	v_exp_f32_e32 v156, v156
	v_exp_f32_e32 v157, v157
	v_exp_f32_e32 v158, v158
	v_exp_f32_e32 v159, v159
	v_exp_f32_e32 v160, v160
	v_exp_f32_e32 v161, v161
	v_exp_f32_e32 v162, v162
	v_exp_f32_e32 v163, v163
	v_exp_f32_e32 v164, v164
	v_exp_f32_e32 v165, v165
	v_pk_add_f32 v[150:151], v[150:151], 1.0 op_sel_hi:[1,0]
	v_pk_add_f32 v[152:153], v[152:153], 1.0 op_sel_hi:[1,0]
	v_pk_add_f32 v[154:155], v[154:155], 1.0 op_sel_hi:[1,0]
	v_pk_add_f32 v[156:157], v[156:157], 1.0 op_sel_hi:[1,0]
	v_pk_add_f32 v[158:159], v[158:159], 1.0 op_sel_hi:[1,0]
	v_pk_add_f32 v[160:161], v[160:161], 1.0 op_sel_hi:[1,0]
	v_pk_add_f32 v[162:163], v[162:163], 1.0 op_sel_hi:[1,0]
	v_pk_add_f32 v[164:165], v[164:165], 1.0 op_sel_hi:[1,0]
	v_rcp_f32_e32 v150, v150
	v_rcp_f32_e32 v151, v151
	v_rcp_f32_e32 v152, v152
	v_rcp_f32_e32 v153, v153
	v_rcp_f32_e32 v154, v154
	v_rcp_f32_e32 v155, v155
	v_rcp_f32_e32 v156, v156
	v_rcp_f32_e32 v157, v157
	v_rcp_f32_e32 v158, v158
	v_rcp_f32_e32 v159, v159
	v_rcp_f32_e32 v160, v160
	v_rcp_f32_e32 v161, v161
	v_rcp_f32_e32 v162, v162
	v_rcp_f32_e32 v163, v163
	v_rcp_f32_e32 v164, v164
	v_rcp_f32_e32 v165, v165
	v_pk_fma_f32 v[150:151], v[150:151], s[6:7], 0.5 op_sel_hi:[1,0,0]
	v_pk_fma_f32 v[152:153], v[152:153], s[6:7], 0.5 op_sel_hi:[1,0,0]
	v_pk_fma_f32 v[154:155], v[154:155], s[6:7], 0.5 op_sel_hi:[1,0,0]
	v_pk_fma_f32 v[156:157], v[156:157], s[6:7], 0.5 op_sel_hi:[1,0,0]
	v_pk_fma_f32 v[158:159], v[158:159], s[6:7], 0.5 op_sel_hi:[1,0,0]
	v_pk_fma_f32 v[160:161], v[160:161], s[6:7], 0.5 op_sel_hi:[1,0,0]
	v_pk_fma_f32 v[162:163], v[162:163], s[6:7], 0.5 op_sel_hi:[1,0,0]
	v_pk_fma_f32 v[164:165], v[164:165], s[6:7], 0.5 op_sel_hi:[1,0,0]
	v_cvt_u32_f32_e32 v158, v158
	v_cvt_u32_f32_e32 v159, v159
	v_cvt_u32_f32_sdwa v160, v160 dst_sel:WORD_1 dst_unused:UNUSED_PAD src0_sel:DWORD
	v_cvt_u32_f32_sdwa v161, v161 dst_sel:BYTE_3 dst_unused:UNUSED_PAD src0_sel:DWORD
	v_cvt_u32_f32_e32 v150, v150
	v_cvt_u32_f32_e32 v151, v151
	v_cvt_u32_f32_sdwa v152, v152 dst_sel:WORD_1 dst_unused:UNUSED_PAD src0_sel:DWORD
	v_cvt_u32_f32_sdwa v153, v153 dst_sel:BYTE_3 dst_unused:UNUSED_PAD src0_sel:DWORD
	v_cvt_u32_f32_e32 v162, v162
	v_cvt_u32_f32_e32 v163, v163
	v_cvt_u32_f32_sdwa v164, v164 dst_sel:WORD_1 dst_unused:UNUSED_PAD src0_sel:DWORD
	v_cvt_u32_f32_sdwa v165, v165 dst_sel:BYTE_3 dst_unused:UNUSED_PAD src0_sel:DWORD
	v_cvt_u32_f32_e32 v154, v154
	v_cvt_u32_f32_e32 v155, v155
	v_cvt_u32_f32_sdwa v156, v156 dst_sel:WORD_1 dst_unused:UNUSED_PAD src0_sel:DWORD
	v_cvt_u32_f32_sdwa v157, v157 dst_sel:BYTE_3 dst_unused:UNUSED_PAD src0_sel:DWORD
	v_lshl_or_b32 v158, v159, 8, v158
	v_lshl_or_b32 v150, v151, 8, v150
	v_lshl_or_b32 v162, v163, 8, v162
	v_lshl_or_b32 v154, v155, 8, v154
	v_or3_b32 v158, v158, v160, v161
	v_or3_b32 v159, v150, v152, v153
	v_or3_b32 v160, v162, v164, v165
	v_or3_b32 v161, v154, v156, v157
	s_nop 1
	v_permlane16_swap_b32_e32 v158, v160
	v_permlane16_swap_b32_e32 v159, v161
	global_store_dwordx4 v[12:13], v[158:161], off
	v_pk_mul_f32 v[134:135], v[134:135], s[4:5] op_sel_hi:[1,0]
	v_pk_mul_f32 v[136:137], v[136:137], s[4:5] op_sel_hi:[1,0]
	v_pk_mul_f32 v[138:139], v[138:139], s[4:5] op_sel_hi:[1,0]
	v_pk_mul_f32 v[140:141], v[140:141], s[4:5] op_sel_hi:[1,0]
	v_pk_mul_f32 v[142:143], v[142:143], s[4:5] op_sel_hi:[1,0]
	v_pk_mul_f32 v[144:145], v[144:145], s[4:5] op_sel_hi:[1,0]
	v_pk_mul_f32 v[146:147], v[146:147], s[4:5] op_sel_hi:[1,0]
	v_pk_mul_f32 v[148:149], v[148:149], s[4:5] op_sel_hi:[1,0]
	v_exp_f32_e32 v134, v134
	v_exp_f32_e32 v135, v135
	v_exp_f32_e32 v136, v136
	v_exp_f32_e32 v137, v137
	v_exp_f32_e32 v138, v138
	v_exp_f32_e32 v139, v139
	v_exp_f32_e32 v140, v140
	v_exp_f32_e32 v141, v141
	v_exp_f32_e32 v142, v142
	v_exp_f32_e32 v143, v143
	v_exp_f32_e32 v144, v144
	v_exp_f32_e32 v145, v145
	v_exp_f32_e32 v146, v146
; DI float sigmoid64_(float x64) { return __builtin_amdgcn_rcpf(1.0f + __builtin_amdgcn_exp2f(x64 * (-LOG2E * W8_INV))); }
;     DI void operator()(const f32x4 (&acc)[2][2][4][2], const Unit& u, int wr, int wc, int fr, int fq) const {
;     ...
;                     for (int m = 0; m < 4; ++m) { unsigned char* rowp = (unsigned char*)gt + (size_t)(row0 + ai * 128 + m * 16) * 2048 + (pn - 30) * 256 + wc * 32 + 8 * fq;
;                         u32x2 o[2];
; #pragma unroll
;                         for (int bj = 0; bj < 2; ++bj) {
; #pragma unroll
;                             for (int n = 0; n < 2; ++n) { const f32x4 v = acc[ai][bj][m][n];
;                                 o[bj][n] = (unsigned)(sigmoid64_(v[0]) * 255.0f + 0.5f) | ((unsigned)(sigmoid64_(v[1]) * 255.0f + 0.5f) << 8) | ((unsigned)(sigmoid64_(v[2]) * 255.0f + 0.5f) << 16) | ((unsigned)(sigmoid64_(v[3]) * 255.0f + 0.5f) << 24); } }
;                         st_pair16(rowp, 128, o[0], o[1], fq); }
	v_exp_f32_e32 v147, v147
	v_exp_f32_e32 v148, v148
	v_exp_f32_e32 v149, v149
	v_pk_add_f32 v[134:135], v[134:135], 1.0 op_sel_hi:[1,0]
	v_pk_add_f32 v[136:137], v[136:137], 1.0 op_sel_hi:[1,0]
	v_pk_add_f32 v[138:139], v[138:139], 1.0 op_sel_hi:[1,0]
	v_pk_add_f32 v[140:141], v[140:141], 1.0 op_sel_hi:[1,0]
	v_pk_add_f32 v[142:143], v[142:143], 1.0 op_sel_hi:[1,0]
	v_pk_add_f32 v[144:145], v[144:145], 1.0 op_sel_hi:[1,0]
	v_pk_add_f32 v[146:147], v[146:147], 1.0 op_sel_hi:[1,0]
	v_pk_add_f32 v[148:149], v[148:149], 1.0 op_sel_hi:[1,0]
	v_rcp_f32_e32 v134, v134
	v_rcp_f32_e32 v135, v135
	v_rcp_f32_e32 v136, v136
	v_rcp_f32_e32 v137, v137
	v_rcp_f32_e32 v138, v138
	v_rcp_f32_e32 v139, v139
	v_rcp_f32_e32 v140, v140
	v_rcp_f32_e32 v141, v141
	v_rcp_f32_e32 v142, v142
	v_rcp_f32_e32 v143, v143
	v_rcp_f32_e32 v144, v144
	v_rcp_f32_e32 v145, v145
	v_rcp_f32_e32 v146, v146
	v_rcp_f32_e32 v147, v147
	v_rcp_f32_e32 v148, v148
	v_rcp_f32_e32 v149, v149
	v_pk_fma_f32 v[134:135], v[134:135], s[6:7], 0.5 op_sel_hi:[1,0,0]
	v_pk_fma_f32 v[136:137], v[136:137], s[6:7], 0.5 op_sel_hi:[1,0,0]
	v_pk_fma_f32 v[138:139], v[138:139], s[6:7], 0.5 op_sel_hi:[1,0,0]
	v_pk_fma_f32 v[140:141], v[140:141], s[6:7], 0.5 op_sel_hi:[1,0,0]
	v_pk_fma_f32 v[142:143], v[142:143], s[6:7], 0.5 op_sel_hi:[1,0,0]
	v_pk_fma_f32 v[144:145], v[144:145], s[6:7], 0.5 op_sel_hi:[1,0,0]
	v_pk_fma_f32 v[146:147], v[146:147], s[6:7], 0.5 op_sel_hi:[1,0,0]
	v_pk_fma_f32 v[148:149], v[148:149], s[6:7], 0.5 op_sel_hi:[1,0,0]
	v_cvt_u32_f32_e32 v142, v142
	v_cvt_u32_f32_e32 v143, v143
	v_cvt_u32_f32_sdwa v144, v144 dst_sel:WORD_1 dst_unused:UNUSED_PAD src0_sel:DWORD
	v_cvt_u32_f32_sdwa v145, v145 dst_sel:BYTE_3 dst_unused:UNUSED_PAD src0_sel:DWORD
	v_cvt_u32_f32_e32 v134, v134
	v_cvt_u32_f32_e32 v135, v135
	v_cvt_u32_f32_sdwa v136, v136 dst_sel:WORD_1 dst_unused:UNUSED_PAD src0_sel:DWORD
	v_cvt_u32_f32_sdwa v137, v137 dst_sel:BYTE_3 dst_unused:UNUSED_PAD src0_sel:DWORD
	v_cvt_u32_f32_e32 v146, v146
	v_cvt_u32_f32_e32 v147, v147
	v_cvt_u32_f32_sdwa v148, v148 dst_sel:WORD_1 dst_unused:UNUSED_PAD src0_sel:DWORD
	v_cvt_u32_f32_sdwa v149, v149 dst_sel:BYTE_3 dst_unused:UNUSED_PAD src0_sel:DWORD
	v_cvt_u32_f32_e32 v138, v138
	v_cvt_u32_f32_e32 v139, v139
	v_cvt_u32_f32_sdwa v140, v140 dst_sel:WORD_1 dst_unused:UNUSED_PAD src0_sel:DWORD
	v_cvt_u32_f32_sdwa v141, v141 dst_sel:BYTE_3 dst_unused:UNUSED_PAD src0_sel:DWORD
	v_lshl_or_b32 v142, v143, 8, v142
	v_lshl_or_b32 v134, v135, 8, v134
	v_lshl_or_b32 v146, v147, 8, v146
	v_lshl_or_b32 v138, v139, 8, v138
	v_or3_b32 v142, v142, v144, v145
	v_or3_b32 v143, v134, v136, v137
	v_or3_b32 v144, v146, v148, v149
	v_or3_b32 v145, v138, v140, v141
	v_add_co_u32_e32 v14, vcc, 0x8000, v12
	s_nop 0
	v_permlane16_swap_b32_e32 v142, v144
	v_addc_co_u32_e32 v15, vcc, 0, v13, vcc
	v_permlane16_swap_b32_e32 v143, v145
	global_store_dwordx4 v[14:15], v[142:145], off
	v_pk_mul_f32 v[118:119], v[118:119], s[4:5] op_sel_hi:[1,0]
	v_pk_mul_f32 v[120:121], v[120:121], s[4:5] op_sel_hi:[1,0]
	v_pk_mul_f32 v[122:123], v[122:123], s[4:5] op_sel_hi:[1,0]
	v_pk_mul_f32 v[124:125], v[124:125], s[4:5] op_sel_hi:[1,0]
	v_pk_mul_f32 v[126:127], v[126:127], s[4:5] op_sel_hi:[1,0]
	v_pk_mul_f32 v[128:129], v[128:129], s[4:5] op_sel_hi:[1,0]
	v_pk_mul_f32 v[130:131], v[130:131], s[4:5] op_sel_hi:[1,0]
	v_pk_mul_f32 v[132:133], v[132:133], s[4:5] op_sel_hi:[1,0]
	v_exp_f32_e32 v118, v118
	v_exp_f32_e32 v119, v119
	v_exp_f32_e32 v120, v120
	v_exp_f32_e32 v121, v121
	v_exp_f32_e32 v122, v122
	v_exp_f32_e32 v123, v123
	v_exp_f32_e32 v124, v124
	v_exp_f32_e32 v125, v125
	v_exp_f32_e32 v126, v126
	v_exp_f32_e32 v127, v127
	v_exp_f32_e32 v128, v128
	v_exp_f32_e32 v129, v129
	v_exp_f32_e32 v130, v130
	v_exp_f32_e32 v131, v131
	v_exp_f32_e32 v132, v132
	v_exp_f32_e32 v133, v133
	v_pk_add_f32 v[118:119], v[118:119], 1.0 op_sel_hi:[1,0]
	v_pk_add_f32 v[120:121], v[120:121], 1.0 op_sel_hi:[1,0]
	v_pk_add_f32 v[122:123], v[122:123], 1.0 op_sel_hi:[1,0]
	v_pk_add_f32 v[124:125], v[124:125], 1.0 op_sel_hi:[1,0]
	v_pk_add_f32 v[126:127], v[126:127], 1.0 op_sel_hi:[1,0]
	v_pk_add_f32 v[128:129], v[128:129], 1.0 op_sel_hi:[1,0]
	v_pk_add_f32 v[130:131], v[130:131], 1.0 op_sel_hi:[1,0]
	v_pk_add_f32 v[132:133], v[132:133], 1.0 op_sel_hi:[1,0]
	v_rcp_f32_e32 v118, v118
	v_rcp_f32_e32 v119, v119
	v_rcp_f32_e32 v120, v120
	v_rcp_f32_e32 v121, v121
	v_rcp_f32_e32 v122, v122
	v_rcp_f32_e32 v123, v123
	v_rcp_f32_e32 v124, v124
	v_rcp_f32_e32 v125, v125
	v_rcp_f32_e32 v126, v126
	v_rcp_f32_e32 v127, v127
	v_rcp_f32_e32 v128, v128
	v_rcp_f32_e32 v129, v129
	v_rcp_f32_e32 v130, v130
	v_rcp_f32_e32 v131, v131
	v_rcp_f32_e32 v132, v132
	v_rcp_f32_e32 v133, v133
	v_pk_fma_f32 v[118:119], v[118:119], s[6:7], 0.5 op_sel_hi:[1,0,0]
	v_pk_fma_f32 v[120:121], v[120:121], s[6:7], 0.5 op_sel_hi:[1,0,0]
	v_pk_fma_f32 v[122:123], v[122:123], s[6:7], 0.5 op_sel_hi:[1,0,0]
	v_pk_fma_f32 v[124:125], v[124:125], s[6:7], 0.5 op_sel_hi:[1,0,0]
	v_pk_fma_f32 v[126:127], v[126:127], s[6:7], 0.5 op_sel_hi:[1,0,0]
	v_pk_fma_f32 v[128:129], v[128:129], s[6:7], 0.5 op_sel_hi:[1,0,0]
	v_pk_fma_f32 v[130:131], v[130:131], s[6:7], 0.5 op_sel_hi:[1,0,0]
	v_pk_fma_f32 v[132:133], v[132:133], s[6:7], 0.5 op_sel_hi:[1,0,0]
	v_cvt_u32_f32_e32 v126, v126
	v_cvt_u32_f32_e32 v127, v127
	v_cvt_u32_f32_sdwa v128, v128 dst_sel:WORD_1 dst_unused:UNUSED_PAD src0_sel:DWORD
	v_cvt_u32_f32_sdwa v129, v129 dst_sel:BYTE_3 dst_unused:UNUSED_PAD src0_sel:DWORD
	v_cvt_u32_f32_e32 v118, v118
	v_cvt_u32_f32_e32 v119, v119
	v_cvt_u32_f32_sdwa v120, v120 dst_sel:WORD_1 dst_unused:UNUSED_PAD src0_sel:DWORD
	v_cvt_u32_f32_sdwa v121, v121 dst_sel:BYTE_3 dst_unused:UNUSED_PAD src0_sel:DWORD
; DI float sigmoid64_(float x64) { return __builtin_amdgcn_rcpf(1.0f + __builtin_amdgcn_exp2f(x64 * (-LOG2E * W8_INV))); }
;     DI void operator()(const f32x4 (&acc)[2][2][4][2], const Unit& u, int wr, int wc, int fr, int fq) const {
;     ...
;                     for (int m = 0; m < 4; ++m) { unsigned char* rowp = (unsigned char*)gt + (size_t)(row0 + ai * 128 + m * 16) * 2048 + (pn - 30) * 256 + wc * 32 + 8 * fq;
;                         u32x2 o[2];
; #pragma unroll
;                         for (int bj = 0; bj < 2; ++bj) {
; #pragma unroll
;                             for (int n = 0; n < 2; ++n) { const f32x4 v = acc[ai][bj][m][n];
;                                 o[bj][n] = (unsigned)(sigmoid64_(v[0]) * 255.0f + 0.5f) | ((unsigned)(sigmoid64_(v[1]) * 255.0f + 0.5f) << 8) | ((unsigned)(sigmoid64_(v[2]) * 255.0f + 0.5f) << 16) | ((unsigned)(sigmoid64_(v[3]) * 255.0f + 0.5f) << 24); } }
;                         st_pair16(rowp, 128, o[0], o[1], fq); }
	v_cvt_u32_f32_e32 v130, v130
	v_cvt_u32_f32_e32 v131, v131
	v_cvt_u32_f32_sdwa v132, v132 dst_sel:WORD_1 dst_unused:UNUSED_PAD src0_sel:DWORD
	v_cvt_u32_f32_sdwa v133, v133 dst_sel:BYTE_3 dst_unused:UNUSED_PAD src0_sel:DWORD
	v_cvt_u32_f32_e32 v122, v122
	v_cvt_u32_f32_e32 v123, v123
	v_cvt_u32_f32_sdwa v124, v124 dst_sel:WORD_1 dst_unused:UNUSED_PAD src0_sel:DWORD
	v_cvt_u32_f32_sdwa v125, v125 dst_sel:BYTE_3 dst_unused:UNUSED_PAD src0_sel:DWORD
	v_lshl_or_b32 v126, v127, 8, v126
	v_lshl_or_b32 v118, v119, 8, v118
	v_lshl_or_b32 v130, v131, 8, v130
	v_lshl_or_b32 v122, v123, 8, v122
	v_or3_b32 v126, v126, v128, v129
	v_or3_b32 v127, v118, v120, v121
	v_or3_b32 v128, v130, v132, v133
	v_or3_b32 v129, v122, v124, v125
	v_add_co_u32_e32 v14, vcc, 0x10000, v12
	s_nop 0
	v_permlane16_swap_b32_e32 v126, v128
	v_addc_co_u32_e32 v15, vcc, 0, v13, vcc
	v_permlane16_swap_b32_e32 v127, v129
	global_store_dwordx4 v[14:15], v[126:129], off
	v_pk_mul_f32 v[102:103], v[102:103], s[4:5] op_sel_hi:[1,0]
	v_pk_mul_f32 v[104:105], v[104:105], s[4:5] op_sel_hi:[1,0]
	v_pk_mul_f32 v[106:107], v[106:107], s[4:5] op_sel_hi:[1,0]
	v_pk_mul_f32 v[108:109], v[108:109], s[4:5] op_sel_hi:[1,0]
	v_pk_mul_f32 v[110:111], v[110:111], s[4:5] op_sel_hi:[1,0]
	v_pk_mul_f32 v[112:113], v[112:113], s[4:5] op_sel_hi:[1,0]
	v_pk_mul_f32 v[114:115], v[114:115], s[4:5] op_sel_hi:[1,0]
	v_pk_mul_f32 v[116:117], v[116:117], s[4:5] op_sel_hi:[1,0]
	v_exp_f32_e32 v102, v102
	v_exp_f32_e32 v103, v103
	v_exp_f32_e32 v104, v104
	v_exp_f32_e32 v105, v105
	v_exp_f32_e32 v106, v106
	v_exp_f32_e32 v107, v107
	v_exp_f32_e32 v108, v108
	v_exp_f32_e32 v109, v109
	v_exp_f32_e32 v110, v110
	v_exp_f32_e32 v111, v111
	v_exp_f32_e32 v112, v112
	v_exp_f32_e32 v113, v113
	v_exp_f32_e32 v114, v114
	v_exp_f32_e32 v115, v115
	v_exp_f32_e32 v116, v116
	v_exp_f32_e32 v117, v117
	v_pk_add_f32 v[102:103], v[102:103], 1.0 op_sel_hi:[1,0]
	v_pk_add_f32 v[104:105], v[104:105], 1.0 op_sel_hi:[1,0]
	v_pk_add_f32 v[106:107], v[106:107], 1.0 op_sel_hi:[1,0]
	v_pk_add_f32 v[108:109], v[108:109], 1.0 op_sel_hi:[1,0]
	v_pk_add_f32 v[110:111], v[110:111], 1.0 op_sel_hi:[1,0]
	v_pk_add_f32 v[112:113], v[112:113], 1.0 op_sel_hi:[1,0]
	v_pk_add_f32 v[114:115], v[114:115], 1.0 op_sel_hi:[1,0]
	v_pk_add_f32 v[116:117], v[116:117], 1.0 op_sel_hi:[1,0]
	v_rcp_f32_e32 v102, v102
	v_rcp_f32_e32 v103, v103
	v_rcp_f32_e32 v104, v104
	v_rcp_f32_e32 v105, v105
	v_rcp_f32_e32 v106, v106
	v_rcp_f32_e32 v107, v107
	v_rcp_f32_e32 v108, v108
	v_rcp_f32_e32 v109, v109
	v_rcp_f32_e32 v110, v110
	v_rcp_f32_e32 v111, v111
	v_rcp_f32_e32 v112, v112
	v_rcp_f32_e32 v113, v113
	v_rcp_f32_e32 v114, v114
	v_rcp_f32_e32 v115, v115
	v_rcp_f32_e32 v116, v116
	v_rcp_f32_e32 v117, v117
	v_pk_fma_f32 v[102:103], v[102:103], s[6:7], 0.5 op_sel_hi:[1,0,0]
	v_pk_fma_f32 v[104:105], v[104:105], s[6:7], 0.5 op_sel_hi:[1,0,0]
	v_pk_fma_f32 v[106:107], v[106:107], s[6:7], 0.5 op_sel_hi:[1,0,0]
	v_pk_fma_f32 v[108:109], v[108:109], s[6:7], 0.5 op_sel_hi:[1,0,0]
	v_pk_fma_f32 v[110:111], v[110:111], s[6:7], 0.5 op_sel_hi:[1,0,0]
	v_pk_fma_f32 v[112:113], v[112:113], s[6:7], 0.5 op_sel_hi:[1,0,0]
	v_pk_fma_f32 v[114:115], v[114:115], s[6:7], 0.5 op_sel_hi:[1,0,0]
	v_pk_fma_f32 v[116:117], v[116:117], s[6:7], 0.5 op_sel_hi:[1,0,0]
	v_cvt_u32_f32_e32 v110, v110
	v_cvt_u32_f32_e32 v111, v111
	v_cvt_u32_f32_sdwa v112, v112 dst_sel:WORD_1 dst_unused:UNUSED_PAD src0_sel:DWORD
	v_cvt_u32_f32_sdwa v113, v113 dst_sel:BYTE_3 dst_unused:UNUSED_PAD src0_sel:DWORD
	v_cvt_u32_f32_e32 v102, v102
	v_cvt_u32_f32_e32 v103, v103
	v_cvt_u32_f32_sdwa v104, v104 dst_sel:WORD_1 dst_unused:UNUSED_PAD src0_sel:DWORD
	v_cvt_u32_f32_sdwa v105, v105 dst_sel:BYTE_3 dst_unused:UNUSED_PAD src0_sel:DWORD
	v_cvt_u32_f32_e32 v114, v114
	v_cvt_u32_f32_e32 v115, v115
	v_cvt_u32_f32_sdwa v116, v116 dst_sel:WORD_1 dst_unused:UNUSED_PAD src0_sel:DWORD
	v_cvt_u32_f32_sdwa v117, v117 dst_sel:BYTE_3 dst_unused:UNUSED_PAD src0_sel:DWORD
	v_cvt_u32_f32_e32 v106, v106
	v_cvt_u32_f32_e32 v107, v107
	v_cvt_u32_f32_sdwa v108, v108 dst_sel:WORD_1 dst_unused:UNUSED_PAD src0_sel:DWORD
	v_cvt_u32_f32_sdwa v109, v109 dst_sel:BYTE_3 dst_unused:UNUSED_PAD src0_sel:DWORD
	v_lshl_or_b32 v110, v111, 8, v110
	v_lshl_or_b32 v102, v103, 8, v102
	v_lshl_or_b32 v114, v115, 8, v114
	v_lshl_or_b32 v106, v107, 8, v106
	v_or3_b32 v110, v110, v112, v113
	v_or3_b32 v111, v102, v104, v105
	v_or3_b32 v112, v114, v116, v117
	v_or3_b32 v113, v106, v108, v109
	v_add_co_u32_e32 v14, vcc, 0x18000, v12
	s_nop 0
	v_permlane16_swap_b32_e32 v110, v112
	v_addc_co_u32_e32 v15, vcc, 0, v13, vcc
	v_permlane16_swap_b32_e32 v111, v113
	global_store_dwordx4 v[14:15], v[110:113], off
	v_pk_mul_f32 v[86:87], v[86:87], s[4:5] op_sel_hi:[1,0]
	v_pk_mul_f32 v[88:89], v[88:89], s[4:5] op_sel_hi:[1,0]
	v_pk_mul_f32 v[90:91], v[90:91], s[4:5] op_sel_hi:[1,0]
	v_pk_mul_f32 v[92:93], v[92:93], s[4:5] op_sel_hi:[1,0]
	v_pk_mul_f32 v[94:95], v[94:95], s[4:5] op_sel_hi:[1,0]
	v_pk_mul_f32 v[96:97], v[96:97], s[4:5] op_sel_hi:[1,0]
	v_pk_mul_f32 v[98:99], v[98:99], s[4:5] op_sel_hi:[1,0]
	v_pk_mul_f32 v[100:101], v[100:101], s[4:5] op_sel_hi:[1,0]
	v_exp_f32_e32 v86, v86
	v_exp_f32_e32 v87, v87
	v_exp_f32_e32 v88, v88
	v_exp_f32_e32 v89, v89
	v_exp_f32_e32 v90, v90
	v_exp_f32_e32 v91, v91
	v_exp_f32_e32 v92, v92
	v_exp_f32_e32 v93, v93
	v_exp_f32_e32 v94, v94
	v_exp_f32_e32 v95, v95
	v_exp_f32_e32 v96, v96
	v_exp_f32_e32 v97, v97
	v_exp_f32_e32 v98, v98
	v_exp_f32_e32 v99, v99
	v_exp_f32_e32 v100, v100
	v_exp_f32_e32 v101, v101
	v_pk_add_f32 v[86:87], v[86:87], 1.0 op_sel_hi:[1,0]
	v_pk_add_f32 v[88:89], v[88:89], 1.0 op_sel_hi:[1,0]
; DI float sigmoid64_(float x64) { return __builtin_amdgcn_rcpf(1.0f + __builtin_amdgcn_exp2f(x64 * (-LOG2E * W8_INV))); }
;     DI void operator()(const f32x4 (&acc)[2][2][4][2], const Unit& u, int wr, int wc, int fr, int fq) const {
;     ...
;                     for (int m = 0; m < 4; ++m) { unsigned char* rowp = (unsigned char*)gt + (size_t)(row0 + ai * 128 + m * 16) * 2048 + (pn - 30) * 256 + wc * 32 + 8 * fq;
;                         u32x2 o[2];
; #pragma unroll
;                         for (int bj = 0; bj < 2; ++bj) {
; #pragma unroll
;                             for (int n = 0; n < 2; ++n) { const f32x4 v = acc[ai][bj][m][n];
;                                 o[bj][n] = (unsigned)(sigmoid64_(v[0]) * 255.0f + 0.5f) | ((unsigned)(sigmoid64_(v[1]) * 255.0f + 0.5f) << 8) | ((unsigned)(sigmoid64_(v[2]) * 255.0f + 0.5f) << 16) | ((unsigned)(sigmoid64_(v[3]) * 255.0f + 0.5f) << 24); } }
;                         st_pair16(rowp, 128, o[0], o[1], fq); }
	v_pk_add_f32 v[90:91], v[90:91], 1.0 op_sel_hi:[1,0]
	v_pk_add_f32 v[92:93], v[92:93], 1.0 op_sel_hi:[1,0]
	v_pk_add_f32 v[94:95], v[94:95], 1.0 op_sel_hi:[1,0]
	v_pk_add_f32 v[96:97], v[96:97], 1.0 op_sel_hi:[1,0]
	v_pk_add_f32 v[98:99], v[98:99], 1.0 op_sel_hi:[1,0]
	v_pk_add_f32 v[100:101], v[100:101], 1.0 op_sel_hi:[1,0]
	v_rcp_f32_e32 v86, v86
	v_rcp_f32_e32 v87, v87
	v_rcp_f32_e32 v88, v88
	v_rcp_f32_e32 v89, v89
	v_rcp_f32_e32 v90, v90
	v_rcp_f32_e32 v91, v91
	v_rcp_f32_e32 v92, v92
	v_rcp_f32_e32 v93, v93
	v_rcp_f32_e32 v94, v94
	v_rcp_f32_e32 v95, v95
	v_rcp_f32_e32 v96, v96
	v_rcp_f32_e32 v97, v97
	v_rcp_f32_e32 v98, v98
	v_rcp_f32_e32 v99, v99
	v_rcp_f32_e32 v100, v100
	v_rcp_f32_e32 v101, v101
	v_pk_fma_f32 v[86:87], v[86:87], s[6:7], 0.5 op_sel_hi:[1,0,0]
	v_pk_fma_f32 v[88:89], v[88:89], s[6:7], 0.5 op_sel_hi:[1,0,0]
	v_pk_fma_f32 v[90:91], v[90:91], s[6:7], 0.5 op_sel_hi:[1,0,0]
	v_pk_fma_f32 v[92:93], v[92:93], s[6:7], 0.5 op_sel_hi:[1,0,0]
	v_pk_fma_f32 v[94:95], v[94:95], s[6:7], 0.5 op_sel_hi:[1,0,0]
	v_pk_fma_f32 v[96:97], v[96:97], s[6:7], 0.5 op_sel_hi:[1,0,0]
	v_pk_fma_f32 v[98:99], v[98:99], s[6:7], 0.5 op_sel_hi:[1,0,0]
	v_pk_fma_f32 v[100:101], v[100:101], s[6:7], 0.5 op_sel_hi:[1,0,0]
	v_cvt_u32_f32_e32 v94, v94
	v_cvt_u32_f32_e32 v95, v95
	v_cvt_u32_f32_sdwa v96, v96 dst_sel:WORD_1 dst_unused:UNUSED_PAD src0_sel:DWORD
	v_cvt_u32_f32_sdwa v97, v97 dst_sel:BYTE_3 dst_unused:UNUSED_PAD src0_sel:DWORD
	v_cvt_u32_f32_e32 v86, v86
	v_cvt_u32_f32_e32 v87, v87
	v_cvt_u32_f32_sdwa v88, v88 dst_sel:WORD_1 dst_unused:UNUSED_PAD src0_sel:DWORD
	v_cvt_u32_f32_sdwa v89, v89 dst_sel:BYTE_3 dst_unused:UNUSED_PAD src0_sel:DWORD
	v_cvt_u32_f32_e32 v98, v98
	v_cvt_u32_f32_e32 v99, v99
	v_cvt_u32_f32_sdwa v100, v100 dst_sel:WORD_1 dst_unused:UNUSED_PAD src0_sel:DWORD
	v_cvt_u32_f32_sdwa v101, v101 dst_sel:BYTE_3 dst_unused:UNUSED_PAD src0_sel:DWORD
	v_cvt_u32_f32_e32 v90, v90
	v_cvt_u32_f32_e32 v91, v91
	v_cvt_u32_f32_sdwa v92, v92 dst_sel:WORD_1 dst_unused:UNUSED_PAD src0_sel:DWORD
	v_cvt_u32_f32_sdwa v93, v93 dst_sel:BYTE_3 dst_unused:UNUSED_PAD src0_sel:DWORD
	v_lshl_or_b32 v94, v95, 8, v94
	v_lshl_or_b32 v86, v87, 8, v86
	v_lshl_or_b32 v98, v99, 8, v98
	v_lshl_or_b32 v90, v91, 8, v90
	v_or3_b32 v94, v94, v96, v97
	v_or3_b32 v95, v86, v88, v89
	v_or3_b32 v96, v98, v100, v101
	v_or3_b32 v97, v90, v92, v93
	v_add_co_u32_e32 v14, vcc, 0x40000, v12
	s_nop 0
	v_permlane16_swap_b32_e32 v94, v96
	v_addc_co_u32_e32 v15, vcc, 0, v13, vcc
	v_permlane16_swap_b32_e32 v95, v97
	global_store_dwordx4 v[14:15], v[94:97], off
	v_pk_mul_f32 v[70:71], v[70:71], s[4:5] op_sel_hi:[1,0]
	v_pk_mul_f32 v[72:73], v[72:73], s[4:5] op_sel_hi:[1,0]
	v_pk_mul_f32 v[74:75], v[74:75], s[4:5] op_sel_hi:[1,0]
	v_pk_mul_f32 v[76:77], v[76:77], s[4:5] op_sel_hi:[1,0]
	v_pk_mul_f32 v[78:79], v[78:79], s[4:5] op_sel_hi:[1,0]
	v_pk_mul_f32 v[80:81], v[80:81], s[4:5] op_sel_hi:[1,0]
	v_pk_mul_f32 v[82:83], v[82:83], s[4:5] op_sel_hi:[1,0]
	v_pk_mul_f32 v[84:85], v[84:85], s[4:5] op_sel_hi:[1,0]
	v_exp_f32_e32 v70, v70
	v_exp_f32_e32 v71, v71
	v_exp_f32_e32 v72, v72
	v_exp_f32_e32 v73, v73
	v_exp_f32_e32 v74, v74
	v_exp_f32_e32 v75, v75
	v_exp_f32_e32 v76, v76
	v_exp_f32_e32 v77, v77
	v_exp_f32_e32 v78, v78
	v_exp_f32_e32 v79, v79
	v_exp_f32_e32 v80, v80
	v_exp_f32_e32 v81, v81
	v_exp_f32_e32 v82, v82
	v_exp_f32_e32 v83, v83
	v_exp_f32_e32 v84, v84
	v_exp_f32_e32 v85, v85
	v_pk_add_f32 v[70:71], v[70:71], 1.0 op_sel_hi:[1,0]
	v_pk_add_f32 v[72:73], v[72:73], 1.0 op_sel_hi:[1,0]
	v_pk_add_f32 v[74:75], v[74:75], 1.0 op_sel_hi:[1,0]
	v_pk_add_f32 v[76:77], v[76:77], 1.0 op_sel_hi:[1,0]
	v_pk_add_f32 v[78:79], v[78:79], 1.0 op_sel_hi:[1,0]
	v_pk_add_f32 v[80:81], v[80:81], 1.0 op_sel_hi:[1,0]
	v_pk_add_f32 v[82:83], v[82:83], 1.0 op_sel_hi:[1,0]
	v_pk_add_f32 v[84:85], v[84:85], 1.0 op_sel_hi:[1,0]
	v_rcp_f32_e32 v70, v70
	v_rcp_f32_e32 v71, v71
	v_rcp_f32_e32 v72, v72
	v_rcp_f32_e32 v73, v73
	v_rcp_f32_e32 v74, v74
	v_rcp_f32_e32 v75, v75
	v_rcp_f32_e32 v76, v76
	v_rcp_f32_e32 v77, v77
	v_rcp_f32_e32 v78, v78
	v_rcp_f32_e32 v79, v79
	v_rcp_f32_e32 v80, v80
	v_rcp_f32_e32 v81, v81
	v_rcp_f32_e32 v82, v82
	v_rcp_f32_e32 v83, v83
	v_rcp_f32_e32 v84, v84
	v_rcp_f32_e32 v85, v85
	v_pk_fma_f32 v[70:71], v[70:71], s[6:7], 0.5 op_sel_hi:[1,0,0]
	v_pk_fma_f32 v[72:73], v[72:73], s[6:7], 0.5 op_sel_hi:[1,0,0]
	v_pk_fma_f32 v[74:75], v[74:75], s[6:7], 0.5 op_sel_hi:[1,0,0]
	v_pk_fma_f32 v[76:77], v[76:77], s[6:7], 0.5 op_sel_hi:[1,0,0]
	v_pk_fma_f32 v[78:79], v[78:79], s[6:7], 0.5 op_sel_hi:[1,0,0]
	v_pk_fma_f32 v[80:81], v[80:81], s[6:7], 0.5 op_sel_hi:[1,0,0]
	v_pk_fma_f32 v[82:83], v[82:83], s[6:7], 0.5 op_sel_hi:[1,0,0]
	v_pk_fma_f32 v[84:85], v[84:85], s[6:7], 0.5 op_sel_hi:[1,0,0]
	v_cvt_u32_f32_e32 v78, v78
	v_cvt_u32_f32_e32 v79, v79
	v_cvt_u32_f32_sdwa v80, v80 dst_sel:WORD_1 dst_unused:UNUSED_PAD src0_sel:DWORD
	v_cvt_u32_f32_sdwa v81, v81 dst_sel:BYTE_3 dst_unused:UNUSED_PAD src0_sel:DWORD
	v_cvt_u32_f32_e32 v70, v70
	v_cvt_u32_f32_e32 v71, v71
	v_cvt_u32_f32_sdwa v72, v72 dst_sel:WORD_1 dst_unused:UNUSED_PAD src0_sel:DWORD
	v_cvt_u32_f32_sdwa v73, v73 dst_sel:BYTE_3 dst_unused:UNUSED_PAD src0_sel:DWORD
	v_cvt_u32_f32_e32 v82, v82
	v_cvt_u32_f32_e32 v83, v83
	v_cvt_u32_f32_sdwa v84, v84 dst_sel:WORD_1 dst_unused:UNUSED_PAD src0_sel:DWORD
	v_cvt_u32_f32_sdwa v85, v85 dst_sel:BYTE_3 dst_unused:UNUSED_PAD src0_sel:DWORD
	v_cvt_u32_f32_e32 v74, v74
	v_cvt_u32_f32_e32 v75, v75
	v_cvt_u32_f32_sdwa v76, v76 dst_sel:WORD_1 dst_unused:UNUSED_PAD src0_sel:DWORD
	v_cvt_u32_f32_sdwa v77, v77 dst_sel:BYTE_3 dst_unused:UNUSED_PAD src0_sel:DWORD
	v_lshl_or_b32 v78, v79, 8, v78
; DI float sigmoid64_(float x64) { return __builtin_amdgcn_rcpf(1.0f + __builtin_amdgcn_exp2f(x64 * (-LOG2E * W8_INV))); }
;     DI void operator()(const f32x4 (&acc)[2][2][4][2], const Unit& u, int wr, int wc, int fr, int fq) const {
;     ...
;                     for (int m = 0; m < 4; ++m) { unsigned char* rowp = (unsigned char*)gt + (size_t)(row0 + ai * 128 + m * 16) * 2048 + (pn - 30) * 256 + wc * 32 + 8 * fq;
;                         u32x2 o[2];
; #pragma unroll
;                         for (int bj = 0; bj < 2; ++bj) {
; #pragma unroll
;                             for (int n = 0; n < 2; ++n) { const f32x4 v = acc[ai][bj][m][n];
;                                 o[bj][n] = (unsigned)(sigmoid64_(v[0]) * 255.0f + 0.5f) | ((unsigned)(sigmoid64_(v[1]) * 255.0f + 0.5f) << 8) | ((unsigned)(sigmoid64_(v[2]) * 255.0f + 0.5f) << 16) | ((unsigned)(sigmoid64_(v[3]) * 255.0f + 0.5f) << 24); } }
;                         st_pair16(rowp, 128, o[0], o[1], fq); }
	v_lshl_or_b32 v70, v71, 8, v70
	v_lshl_or_b32 v82, v83, 8, v82
	v_lshl_or_b32 v74, v75, 8, v74
	v_or3_b32 v78, v78, v80, v81
	v_or3_b32 v79, v70, v72, v73
	v_or3_b32 v80, v82, v84, v85
	v_or3_b32 v81, v74, v76, v77
	v_add_co_u32_e32 v14, vcc, 0x48000, v12
	s_nop 0
	v_permlane16_swap_b32_e32 v78, v80
	v_addc_co_u32_e32 v15, vcc, 0, v13, vcc
	v_permlane16_swap_b32_e32 v79, v81
	global_store_dwordx4 v[14:15], v[78:81], off
	v_pk_mul_f32 v[54:55], v[54:55], s[4:5] op_sel_hi:[1,0]
	v_pk_mul_f32 v[56:57], v[56:57], s[4:5] op_sel_hi:[1,0]
	v_pk_mul_f32 v[58:59], v[58:59], s[4:5] op_sel_hi:[1,0]
	v_pk_mul_f32 v[60:61], v[60:61], s[4:5] op_sel_hi:[1,0]
	v_pk_mul_f32 v[62:63], v[62:63], s[4:5] op_sel_hi:[1,0]
	v_pk_mul_f32 v[64:65], v[64:65], s[4:5] op_sel_hi:[1,0]
	v_pk_mul_f32 v[66:67], v[66:67], s[4:5] op_sel_hi:[1,0]
	v_pk_mul_f32 v[68:69], v[68:69], s[4:5] op_sel_hi:[1,0]
	v_exp_f32_e32 v54, v54
	v_exp_f32_e32 v55, v55
	v_exp_f32_e32 v56, v56
	v_exp_f32_e32 v57, v57
	v_exp_f32_e32 v58, v58
	v_exp_f32_e32 v59, v59
	v_exp_f32_e32 v60, v60
	v_exp_f32_e32 v61, v61
	v_exp_f32_e32 v62, v62
	v_exp_f32_e32 v63, v63
	v_exp_f32_e32 v64, v64
	v_exp_f32_e32 v65, v65
	v_exp_f32_e32 v66, v66
	v_exp_f32_e32 v67, v67
	v_exp_f32_e32 v68, v68
	v_exp_f32_e32 v69, v69
	v_pk_add_f32 v[54:55], v[54:55], 1.0 op_sel_hi:[1,0]
	v_pk_add_f32 v[56:57], v[56:57], 1.0 op_sel_hi:[1,0]
	v_pk_add_f32 v[58:59], v[58:59], 1.0 op_sel_hi:[1,0]
	v_pk_add_f32 v[60:61], v[60:61], 1.0 op_sel_hi:[1,0]
	v_pk_add_f32 v[62:63], v[62:63], 1.0 op_sel_hi:[1,0]
	v_pk_add_f32 v[64:65], v[64:65], 1.0 op_sel_hi:[1,0]
	v_pk_add_f32 v[66:67], v[66:67], 1.0 op_sel_hi:[1,0]
	v_pk_add_f32 v[68:69], v[68:69], 1.0 op_sel_hi:[1,0]
	v_rcp_f32_e32 v54, v54
	v_rcp_f32_e32 v55, v55
	v_rcp_f32_e32 v56, v56
	v_rcp_f32_e32 v57, v57
	v_rcp_f32_e32 v58, v58
	v_rcp_f32_e32 v59, v59
	v_rcp_f32_e32 v60, v60
	v_rcp_f32_e32 v61, v61
	v_rcp_f32_e32 v62, v62
	v_rcp_f32_e32 v63, v63
	v_rcp_f32_e32 v64, v64
	v_rcp_f32_e32 v65, v65
	v_rcp_f32_e32 v66, v66
	v_rcp_f32_e32 v67, v67
	v_rcp_f32_e32 v68, v68
	v_rcp_f32_e32 v69, v69
	v_pk_fma_f32 v[54:55], v[54:55], s[6:7], 0.5 op_sel_hi:[1,0,0]
	v_pk_fma_f32 v[56:57], v[56:57], s[6:7], 0.5 op_sel_hi:[1,0,0]
	v_pk_fma_f32 v[58:59], v[58:59], s[6:7], 0.5 op_sel_hi:[1,0,0]
	v_pk_fma_f32 v[60:61], v[60:61], s[6:7], 0.5 op_sel_hi:[1,0,0]
	v_pk_fma_f32 v[62:63], v[62:63], s[6:7], 0.5 op_sel_hi:[1,0,0]
	v_pk_fma_f32 v[64:65], v[64:65], s[6:7], 0.5 op_sel_hi:[1,0,0]
	v_pk_fma_f32 v[66:67], v[66:67], s[6:7], 0.5 op_sel_hi:[1,0,0]
	v_pk_fma_f32 v[68:69], v[68:69], s[6:7], 0.5 op_sel_hi:[1,0,0]
	v_cvt_u32_f32_e32 v62, v62
	v_cvt_u32_f32_e32 v63, v63
	v_cvt_u32_f32_sdwa v64, v64 dst_sel:WORD_1 dst_unused:UNUSED_PAD src0_sel:DWORD
	v_cvt_u32_f32_sdwa v65, v65 dst_sel:BYTE_3 dst_unused:UNUSED_PAD src0_sel:DWORD
	v_cvt_u32_f32_e32 v54, v54
	v_cvt_u32_f32_e32 v55, v55
	v_cvt_u32_f32_sdwa v56, v56 dst_sel:WORD_1 dst_unused:UNUSED_PAD src0_sel:DWORD
	v_cvt_u32_f32_sdwa v57, v57 dst_sel:BYTE_3 dst_unused:UNUSED_PAD src0_sel:DWORD
	v_cvt_u32_f32_e32 v66, v66
	v_cvt_u32_f32_e32 v67, v67
	v_cvt_u32_f32_sdwa v68, v68 dst_sel:WORD_1 dst_unused:UNUSED_PAD src0_sel:DWORD
	v_cvt_u32_f32_sdwa v69, v69 dst_sel:BYTE_3 dst_unused:UNUSED_PAD src0_sel:DWORD
	v_cvt_u32_f32_e32 v58, v58
	v_cvt_u32_f32_e32 v59, v59
	v_cvt_u32_f32_sdwa v60, v60 dst_sel:WORD_1 dst_unused:UNUSED_PAD src0_sel:DWORD
	v_cvt_u32_f32_sdwa v61, v61 dst_sel:BYTE_3 dst_unused:UNUSED_PAD src0_sel:DWORD
	v_lshl_or_b32 v62, v63, 8, v62
	v_lshl_or_b32 v54, v55, 8, v54
	v_lshl_or_b32 v66, v67, 8, v66
	v_lshl_or_b32 v58, v59, 8, v58
	v_or3_b32 v62, v62, v64, v65
	v_or3_b32 v63, v54, v56, v57
	v_or3_b32 v64, v66, v68, v69
	v_or3_b32 v65, v58, v60, v61
; DI float sigmoid64_(float x64) { return __builtin_amdgcn_rcpf(1.0f + __builtin_amdgcn_exp2f(x64 * (-LOG2E * W8_INV))); }
;     DI void operator()(const f32x4 (&acc)[2][2][4][2], const Unit& u, int wr, int wc, int fr, int fq) const {
;     ...
;                     for (int m = 0; m < 4; ++m) { unsigned char* rowp = (unsigned char*)gt + (size_t)(row0 + ai * 128 + m * 16) * 2048 + (pn - 30) * 256 + wc * 32 + 8 * fq;
;                         u32x2 o[2];
; #pragma unroll
;                         for (int bj = 0; bj < 2; ++bj) {
; #pragma unroll
;                             for (int n = 0; n < 2; ++n) { const f32x4 v = acc[ai][bj][m][n];
;                                 o[bj][n] = (unsigned)(sigmoid64_(v[0]) * 255.0f + 0.5f) | ((unsigned)(sigmoid64_(v[1]) * 255.0f + 0.5f) << 8) | ((unsigned)(sigmoid64_(v[2]) * 255.0f + 0.5f) << 16) | ((unsigned)(sigmoid64_(v[3]) * 255.0f + 0.5f) << 24); } }
;                         st_pair16(rowp, 128, o[0], o[1], fq); }
	v_add_co_u32_e32 v14, vcc, 0x50000, v12
	s_nop 0
	v_permlane16_swap_b32_e32 v62, v64
	v_addc_co_u32_e32 v15, vcc, 0, v13, vcc
	v_permlane16_swap_b32_e32 v63, v65
	global_store_dwordx4 v[14:15], v[62:65], off
	v_pk_mul_f32 v[38:39], v[38:39], s[4:5] op_sel_hi:[1,0]
	v_pk_mul_f32 v[40:41], v[40:41], s[4:5] op_sel_hi:[1,0]
	v_pk_mul_f32 v[42:43], v[42:43], s[4:5] op_sel_hi:[1,0]
	v_pk_mul_f32 v[44:45], v[44:45], s[4:5] op_sel_hi:[1,0]
	v_pk_mul_f32 v[46:47], v[46:47], s[4:5] op_sel_hi:[1,0]
	v_pk_mul_f32 v[48:49], v[48:49], s[4:5] op_sel_hi:[1,0]
	v_pk_mul_f32 v[50:51], v[50:51], s[4:5] op_sel_hi:[1,0]
	v_pk_mul_f32 v[52:53], v[52:53], s[4:5] op_sel_hi:[1,0]
	v_exp_f32_e32 v38, v38
	v_exp_f32_e32 v39, v39
	v_exp_f32_e32 v40, v40
	v_exp_f32_e32 v41, v41
	v_exp_f32_e32 v42, v42
	v_exp_f32_e32 v43, v43
	v_exp_f32_e32 v44, v44
	v_exp_f32_e32 v45, v45
	v_exp_f32_e32 v46, v46
	v_exp_f32_e32 v47, v47
	v_exp_f32_e32 v48, v48
	v_exp_f32_e32 v49, v49
	v_exp_f32_e32 v50, v50
	v_exp_f32_e32 v51, v51
	v_exp_f32_e32 v52, v52
	v_exp_f32_e32 v53, v53
	v_pk_add_f32 v[38:39], v[38:39], 1.0 op_sel_hi:[1,0]
	v_pk_add_f32 v[40:41], v[40:41], 1.0 op_sel_hi:[1,0]
	v_pk_add_f32 v[42:43], v[42:43], 1.0 op_sel_hi:[1,0]
	v_pk_add_f32 v[44:45], v[44:45], 1.0 op_sel_hi:[1,0]
	v_pk_add_f32 v[46:47], v[46:47], 1.0 op_sel_hi:[1,0]
	v_pk_add_f32 v[48:49], v[48:49], 1.0 op_sel_hi:[1,0]
	v_pk_add_f32 v[50:51], v[50:51], 1.0 op_sel_hi:[1,0]
	v_pk_add_f32 v[52:53], v[52:53], 1.0 op_sel_hi:[1,0]
	v_rcp_f32_e32 v38, v38
	v_rcp_f32_e32 v39, v39
	v_rcp_f32_e32 v40, v40
	v_rcp_f32_e32 v41, v41
	v_rcp_f32_e32 v42, v42
	v_rcp_f32_e32 v43, v43
	v_rcp_f32_e32 v44, v44
	v_rcp_f32_e32 v45, v45
	v_rcp_f32_e32 v46, v46
	v_rcp_f32_e32 v47, v47
	v_rcp_f32_e32 v48, v48
	v_rcp_f32_e32 v49, v49
	v_rcp_f32_e32 v50, v50
	v_rcp_f32_e32 v51, v51
	v_rcp_f32_e32 v52, v52
	v_rcp_f32_e32 v53, v53
	v_pk_fma_f32 v[38:39], v[38:39], s[6:7], 0.5 op_sel_hi:[1,0,0]
	v_pk_fma_f32 v[40:41], v[40:41], s[6:7], 0.5 op_sel_hi:[1,0,0]
	v_pk_fma_f32 v[42:43], v[42:43], s[6:7], 0.5 op_sel_hi:[1,0,0]
	v_pk_fma_f32 v[44:45], v[44:45], s[6:7], 0.5 op_sel_hi:[1,0,0]
	v_pk_fma_f32 v[46:47], v[46:47], s[6:7], 0.5 op_sel_hi:[1,0,0]
	v_pk_fma_f32 v[48:49], v[48:49], s[6:7], 0.5 op_sel_hi:[1,0,0]
	v_pk_fma_f32 v[50:51], v[50:51], s[6:7], 0.5 op_sel_hi:[1,0,0]
	v_pk_fma_f32 v[52:53], v[52:53], s[6:7], 0.5 op_sel_hi:[1,0,0]
	v_cvt_u32_f32_e32 v46, v46
	v_cvt_u32_f32_e32 v47, v47
	v_cvt_u32_f32_sdwa v48, v48 dst_sel:WORD_1 dst_unused:UNUSED_PAD src0_sel:DWORD
	v_cvt_u32_f32_sdwa v49, v49 dst_sel:BYTE_3 dst_unused:UNUSED_PAD src0_sel:DWORD
	v_cvt_u32_f32_e32 v38, v38
	v_cvt_u32_f32_e32 v39, v39
	v_cvt_u32_f32_sdwa v40, v40 dst_sel:WORD_1 dst_unused:UNUSED_PAD src0_sel:DWORD
	v_cvt_u32_f32_sdwa v41, v41 dst_sel:BYTE_3 dst_unused:UNUSED_PAD src0_sel:DWORD
	v_cvt_u32_f32_e32 v50, v50
	v_cvt_u32_f32_e32 v51, v51
	v_cvt_u32_f32_sdwa v52, v52 dst_sel:WORD_1 dst_unused:UNUSED_PAD src0_sel:DWORD
	v_cvt_u32_f32_sdwa v53, v53 dst_sel:BYTE_3 dst_unused:UNUSED_PAD src0_sel:DWORD
	v_cvt_u32_f32_e32 v42, v42
	v_cvt_u32_f32_e32 v43, v43
	v_cvt_u32_f32_sdwa v44, v44 dst_sel:WORD_1 dst_unused:UNUSED_PAD src0_sel:DWORD
	v_cvt_u32_f32_sdwa v45, v45 dst_sel:BYTE_3 dst_unused:UNUSED_PAD src0_sel:DWORD
	v_lshl_or_b32 v46, v47, 8, v46
	v_lshl_or_b32 v38, v39, 8, v38
	v_lshl_or_b32 v50, v51, 8, v50
	v_lshl_or_b32 v42, v43, 8, v42
	v_or3_b32 v46, v46, v48, v49
	v_or3_b32 v47, v38, v40, v41
	v_or3_b32 v48, v50, v52, v53
	v_or3_b32 v49, v42, v44, v45
	v_add_co_u32_e32 v14, vcc, 0x58000, v12
	s_nop 0
	v_permlane16_swap_b32_e32 v46, v48
	v_addc_co_u32_e32 v15, vcc, 0, v13, vcc
	v_permlane16_swap_b32_e32 v47, v49
	global_store_dwordx4 v[14:15], v[46:49], off

; DI unsigned pk4_fp8(float a, float b, float c_, float d) { int w = 0; w = __builtin_amdgcn_cvt_pk_fp8_f32(clamp8(a), clamp8(b), w, false); w = __builtin_amdgcn_cvt_pk_fp8_f32(clamp8(c_), clamp8(d), w, true); return (unsigned)w; }
; DI float sigmoidf_(float x) { return __builtin_amdgcn_rcpf(1.0f + __builtin_amdgcn_exp2f(-x * LOG2E)); }
;     DI void operator()(const f32x4 (&acc)[2][2][4][2], const Unit& u, int wr, int wc, int fr, int fq) const {
;     ...
;             else if (pn < 12) {
; #pragma unroll
;                 for (int ai = 0; ai < 2; ++ai)
; #pragma unroll
;                     for (int m = 0; m < 4; ++m) { unsigned char* rowp = (unsigned char*)sr + (size_t)(row0 + ai * 128 + m * 16) * 1024 + (pn - 8) * 256 + wc * 32 + 8 * fq;
;                         u32x2 o[2];
; #pragma unroll
;                         for (int bj = 0; bj < 2; ++bj) { const f32x4 v0 = acc[ai][bj][m][0] * W8_INV, v1 = acc[ai][bj][m][1] * W8_INV;
;                             o[bj].x = pk4_fp8(v0[0] * sigmoidf_(v0[0]), v0[1] * sigmoidf_(v0[1]), v0[2] * sigmoidf_(v0[2]), v0[3] * sigmoidf_(v0[3]));
;                             o[bj].y = pk4_fp8(v1[0] * sigmoidf_(v1[0]), v1[1] * sigmoidf_(v1[1]), v1[2] * sigmoidf_(v1[2]), v1[3] * sigmoidf_(v1[3])); }
;                         st_pair16(rowp, 128, o[0], o[1], fq); }
.LBB0_294:
	s_andn2_b64 vcc, exec, s[16:17]
	s_cbranch_vccnz .LBB0_296
	v_bfe_i32 v6, v18, 0, 1
	v_and_b32_e32 v14, 0x78, v6
	v_mov_b32_e32 v15, v4
	v_ashrrev_i32_e32 v11, 31, v10
	v_lshlrev_b64 v[6:7], 10, v[10:11]
	v_readlane_b32 s6, v255, 22
	v_readlane_b32 s7, v255, 23
	s_lshl_b32 s4, s43, 8
	s_addk_i32 s4, 0xf800
	s_ashr_i32 s5, s4, 31
	v_lshl_add_u64 v[6:7], s[6:7], 0, v[6:7]
	v_lshl_add_u64 v[6:7], v[6:7], 0, s[4:5]
	v_readlane_b32 s4, v255, 36
	v_readlane_b32 s5, v255, 37
	s_nop 1
	v_lshl_add_u64 v[16:17], v[6:7], 0, s[4:5]
	v_lshlrev_b32_e32 v12, 3, v18
	v_ashrrev_i32_e32 v13, 31, v12
	v_lshl_add_u64 v[12:13], v[16:17], 0, v[12:13]
	v_lshl_add_u64 v[12:13], v[12:13], 0, v[14:15]
	s_mov_b32 s4, 0xbfb8aa3b
	v_pk_mul_f32 v[150:151], v[150:151], s[34:35] op_sel_hi:[1,0]
	v_pk_mul_f32 v[152:153], v[152:153], s[34:35] op_sel_hi:[1,0]
	v_pk_mul_f32 v[154:155], v[154:155], s[34:35] op_sel_hi:[1,0]
	v_pk_mul_f32 v[156:157], v[156:157], s[34:35] op_sel_hi:[1,0]
	v_pk_mul_f32 v[6:7], v[150:151], s[4:5] op_sel_hi:[1,0]
	v_pk_mul_f32 v[8:9], v[152:153], s[4:5] op_sel_hi:[1,0]
	v_pk_mul_f32 v[20:21], v[154:155], s[4:5] op_sel_hi:[1,0]
	v_pk_mul_f32 v[22:23], v[156:157], s[4:5] op_sel_hi:[1,0]
	v_exp_f32_e32 v6, v6
	v_exp_f32_e32 v7, v7
	v_exp_f32_e32 v8, v8
	v_exp_f32_e32 v9, v9
	v_exp_f32_e32 v20, v20
	v_exp_f32_e32 v21, v21
	v_exp_f32_e32 v22, v22
	v_exp_f32_e32 v23, v23
	v_pk_add_f32 v[6:7], v[6:7], 1.0 op_sel_hi:[1,0]
	v_pk_add_f32 v[8:9], v[8:9], 1.0 op_sel_hi:[1,0]
	v_pk_add_f32 v[20:21], v[20:21], 1.0 op_sel_hi:[1,0]
	v_pk_add_f32 v[22:23], v[22:23], 1.0 op_sel_hi:[1,0]
	v_rcp_f32_e32 v6, v6
	v_rcp_f32_e32 v7, v7
	v_rcp_f32_e32 v8, v8
	v_rcp_f32_e32 v9, v9
	v_rcp_f32_e32 v20, v20
	v_rcp_f32_e32 v21, v21
	v_rcp_f32_e32 v22, v22
	v_rcp_f32_e32 v23, v23
	v_pk_mul_f32 v[150:151], v[150:151], v[6:7]
	v_pk_mul_f32 v[152:153], v[152:153], v[8:9]
	v_pk_mul_f32 v[154:155], v[154:155], v[20:21]
	v_pk_mul_f32 v[156:157], v[156:157], v[22:23]
	v_med3_f32 v150, v150, s35, v225
	v_med3_f32 v151, v151, s35, v225
	v_med3_f32 v152, v152, s35, v225
	v_med3_f32 v153, v153, s35, v225
	v_med3_f32 v154, v154, s35, v225
	v_med3_f32 v155, v155, s35, v225
	v_med3_f32 v156, v156, s35, v225
	v_med3_f32 v157, v157, s35, v225
	v_pk_mul_f32 v[158:159], v[158:159], s[34:35] op_sel_hi:[1,0]
	v_pk_mul_f32 v[160:161], v[160:161], s[34:35] op_sel_hi:[1,0]
	v_pk_mul_f32 v[162:163], v[162:163], s[34:35] op_sel_hi:[1,0]
	v_pk_mul_f32 v[164:165], v[164:165], s[34:35] op_sel_hi:[1,0]
	v_pk_mul_f32 v[6:7], v[158:159], s[4:5] op_sel_hi:[1,0]
	v_pk_mul_f32 v[8:9], v[160:161], s[4:5] op_sel_hi:[1,0]
	v_pk_mul_f32 v[20:21], v[162:163], s[4:5] op_sel_hi:[1,0]
	v_pk_mul_f32 v[22:23], v[164:165], s[4:5] op_sel_hi:[1,0]
	v_exp_f32_e32 v6, v6
	v_exp_f32_e32 v7, v7
	v_exp_f32_e32 v8, v8
	v_exp_f32_e32 v9, v9
	v_exp_f32_e32 v20, v20
	v_exp_f32_e32 v21, v21
	v_exp_f32_e32 v22, v22
	v_exp_f32_e32 v23, v23
	v_pk_add_f32 v[6:7], v[6:7], 1.0 op_sel_hi:[1,0]
	v_pk_add_f32 v[8:9], v[8:9], 1.0 op_sel_hi:[1,0]
	v_pk_add_f32 v[20:21], v[20:21], 1.0 op_sel_hi:[1,0]
	v_pk_add_f32 v[22:23], v[22:23], 1.0 op_sel_hi:[1,0]
	v_rcp_f32_e32 v6, v6
	v_rcp_f32_e32 v7, v7
	v_rcp_f32_e32 v8, v8
	v_rcp_f32_e32 v9, v9
	v_rcp_f32_e32 v20, v20
	v_rcp_f32_e32 v21, v21
	v_rcp_f32_e32 v22, v22
	v_rcp_f32_e32 v23, v23
	v_pk_mul_f32 v[158:159], v[158:159], v[6:7]
	v_pk_mul_f32 v[160:161], v[160:161], v[8:9]
	v_pk_mul_f32 v[162:163], v[162:163], v[20:21]
	v_pk_mul_f32 v[164:165], v[164:165], v[22:23]
	v_med3_f32 v158, v158, s35, v225
	v_med3_f32 v159, v159, s35, v225
	v_med3_f32 v160, v160, s35, v225
	v_med3_f32 v161, v161, s35, v225
	v_med3_f32 v162, v162, s35, v225
	v_med3_f32 v163, v163, s35, v225
	v_med3_f32 v164, v164, s35, v225
	v_med3_f32 v165, v165, s35, v225
	v_cvt_pk_fp8_f32 v158, v158, v159
	v_cvt_pk_fp8_f32 v159, v150, v151
	v_cvt_pk_fp8_f32 v158, v160, v161 op_sel:[0,0,1]
	v_cvt_pk_fp8_f32 v159, v152, v153 op_sel:[0,0,1]
	v_cvt_pk_fp8_f32 v160, v162, v163
	v_cvt_pk_fp8_f32 v161, v154, v155
	v_cvt_pk_fp8_f32 v160, v164, v165 op_sel:[0,0,1]
	v_cvt_pk_fp8_f32 v161, v156, v157 op_sel:[0,0,1]
	s_nop 1
	v_permlane16_swap_b32_e32 v158, v160
	v_permlane16_swap_b32_e32 v159, v161
	global_store_dwordx4 v[12:13], v[158:161], off
	v_pk_mul_f32 v[134:135], v[134:135], s[34:35] op_sel_hi:[1,0]
	v_pk_mul_f32 v[136:137], v[136:137], s[34:35] op_sel_hi:[1,0]
	v_pk_mul_f32 v[138:139], v[138:139], s[34:35] op_sel_hi:[1,0]
	v_pk_mul_f32 v[140:141], v[140:141], s[34:35] op_sel_hi:[1,0]
	v_pk_mul_f32 v[6:7], v[134:135], s[4:5] op_sel_hi:[1,0]
	v_pk_mul_f32 v[8:9], v[136:137], s[4:5] op_sel_hi:[1,0]
	v_pk_mul_f32 v[20:21], v[138:139], s[4:5] op_sel_hi:[1,0]
	v_pk_mul_f32 v[22:23], v[140:141], s[4:5] op_sel_hi:[1,0]
	v_exp_f32_e32 v6, v6
	v_exp_f32_e32 v7, v7
	v_exp_f32_e32 v8, v8
	v_exp_f32_e32 v9, v9
	v_exp_f32_e32 v20, v20
	v_exp_f32_e32 v21, v21
	v_exp_f32_e32 v22, v22
	v_exp_f32_e32 v23, v23
	v_pk_add_f32 v[6:7], v[6:7], 1.0 op_sel_hi:[1,0]
	v_pk_add_f32 v[8:9], v[8:9], 1.0 op_sel_hi:[1,0]
	v_pk_add_f32 v[20:21], v[20:21], 1.0 op_sel_hi:[1,0]
	v_pk_add_f32 v[22:23], v[22:23], 1.0 op_sel_hi:[1,0]
	v_rcp_f32_e32 v6, v6
	v_rcp_f32_e32 v7, v7
	v_rcp_f32_e32 v8, v8
	v_rcp_f32_e32 v9, v9
	v_rcp_f32_e32 v20, v20
	v_rcp_f32_e32 v21, v21
	v_rcp_f32_e32 v22, v22
	v_rcp_f32_e32 v23, v23
	v_pk_mul_f32 v[134:135], v[134:135], v[6:7]
	v_pk_mul_f32 v[136:137], v[136:137], v[8:9]
	v_pk_mul_f32 v[138:139], v[138:139], v[20:21]
	v_pk_mul_f32 v[140:141], v[140:141], v[22:23]
	v_med3_f32 v134, v134, s35, v225
	v_med3_f32 v135, v135, s35, v225
	v_med3_f32 v136, v136, s35, v225
	v_med3_f32 v137, v137, s35, v225
	v_med3_f32 v138, v138, s35, v225
; DI unsigned pk4_fp8(float a, float b, float c_, float d) { int w = 0; w = __builtin_amdgcn_cvt_pk_fp8_f32(clamp8(a), clamp8(b), w, false); w = __builtin_amdgcn_cvt_pk_fp8_f32(clamp8(c_), clamp8(d), w, true); return (unsigned)w; }
; DI float sigmoidf_(float x) { return __builtin_amdgcn_rcpf(1.0f + __builtin_amdgcn_exp2f(-x * LOG2E)); }
;     DI void operator()(const f32x4 (&acc)[2][2][4][2], const Unit& u, int wr, int wc, int fr, int fq) const {
;     ...
;                     for (int m = 0; m < 4; ++m) { unsigned char* rowp = (unsigned char*)sr + (size_t)(row0 + ai * 128 + m * 16) * 1024 + (pn - 8) * 256 + wc * 32 + 8 * fq;
;                         u32x2 o[2];
; #pragma unroll
;                         for (int bj = 0; bj < 2; ++bj) { const f32x4 v0 = acc[ai][bj][m][0] * W8_INV, v1 = acc[ai][bj][m][1] * W8_INV;
;                             o[bj].x = pk4_fp8(v0[0] * sigmoidf_(v0[0]), v0[1] * sigmoidf_(v0[1]), v0[2] * sigmoidf_(v0[2]), v0[3] * sigmoidf_(v0[3]));
;                             o[bj].y = pk4_fp8(v1[0] * sigmoidf_(v1[0]), v1[1] * sigmoidf_(v1[1]), v1[2] * sigmoidf_(v1[2]), v1[3] * sigmoidf_(v1[3])); }
;                         st_pair16(rowp, 128, o[0], o[1], fq); }
	v_med3_f32 v139, v139, s35, v225
	v_med3_f32 v140, v140, s35, v225
	v_med3_f32 v141, v141, s35, v225
	v_pk_mul_f32 v[142:143], v[142:143], s[34:35] op_sel_hi:[1,0]
	v_pk_mul_f32 v[144:145], v[144:145], s[34:35] op_sel_hi:[1,0]
	v_pk_mul_f32 v[146:147], v[146:147], s[34:35] op_sel_hi:[1,0]
	v_pk_mul_f32 v[148:149], v[148:149], s[34:35] op_sel_hi:[1,0]
	v_pk_mul_f32 v[6:7], v[142:143], s[4:5] op_sel_hi:[1,0]
	v_pk_mul_f32 v[8:9], v[144:145], s[4:5] op_sel_hi:[1,0]
	v_pk_mul_f32 v[20:21], v[146:147], s[4:5] op_sel_hi:[1,0]
	v_pk_mul_f32 v[22:23], v[148:149], s[4:5] op_sel_hi:[1,0]
	v_exp_f32_e32 v6, v6
	v_exp_f32_e32 v7, v7
	v_exp_f32_e32 v8, v8
	v_exp_f32_e32 v9, v9
	v_exp_f32_e32 v20, v20
	v_exp_f32_e32 v21, v21
	v_exp_f32_e32 v22, v22
	v_exp_f32_e32 v23, v23
	v_pk_add_f32 v[6:7], v[6:7], 1.0 op_sel_hi:[1,0]
	v_pk_add_f32 v[8:9], v[8:9], 1.0 op_sel_hi:[1,0]
	v_pk_add_f32 v[20:21], v[20:21], 1.0 op_sel_hi:[1,0]
	v_pk_add_f32 v[22:23], v[22:23], 1.0 op_sel_hi:[1,0]
	v_rcp_f32_e32 v6, v6
	v_rcp_f32_e32 v7, v7
	v_rcp_f32_e32 v8, v8
	v_rcp_f32_e32 v9, v9
	v_rcp_f32_e32 v20, v20
	v_rcp_f32_e32 v21, v21
	v_rcp_f32_e32 v22, v22
	v_rcp_f32_e32 v23, v23
	v_pk_mul_f32 v[142:143], v[142:143], v[6:7]
	v_pk_mul_f32 v[144:145], v[144:145], v[8:9]
	v_pk_mul_f32 v[146:147], v[146:147], v[20:21]
	v_pk_mul_f32 v[148:149], v[148:149], v[22:23]
	v_med3_f32 v142, v142, s35, v225
	v_med3_f32 v143, v143, s35, v225
	v_med3_f32 v144, v144, s35, v225
	v_med3_f32 v145, v145, s35, v225
	v_med3_f32 v146, v146, s35, v225
	v_med3_f32 v147, v147, s35, v225
	v_med3_f32 v148, v148, s35, v225
	v_med3_f32 v149, v149, s35, v225
	v_cvt_pk_fp8_f32 v142, v142, v143
	v_cvt_pk_fp8_f32 v143, v134, v135
	v_cvt_pk_fp8_f32 v142, v144, v145 op_sel:[0,0,1]
	v_cvt_pk_fp8_f32 v143, v136, v137 op_sel:[0,0,1]
	v_cvt_pk_fp8_f32 v144, v146, v147
	v_cvt_pk_fp8_f32 v145, v138, v139
	v_cvt_pk_fp8_f32 v144, v148, v149 op_sel:[0,0,1]
	v_cvt_pk_fp8_f32 v145, v140, v141 op_sel:[0,0,1]
	v_add_co_u32_e32 v14, vcc, 0x4000, v12
	s_nop 0
	v_permlane16_swap_b32_e32 v142, v144
	v_addc_co_u32_e32 v15, vcc, 0, v13, vcc
	v_permlane16_swap_b32_e32 v143, v145
	global_store_dwordx4 v[14:15], v[142:145], off
	v_pk_mul_f32 v[118:119], v[118:119], s[34:35] op_sel_hi:[1,0]
	v_pk_mul_f32 v[120:121], v[120:121], s[34:35] op_sel_hi:[1,0]
	v_pk_mul_f32 v[122:123], v[122:123], s[34:35] op_sel_hi:[1,0]
	v_pk_mul_f32 v[124:125], v[124:125], s[34:35] op_sel_hi:[1,0]
	v_pk_mul_f32 v[6:7], v[118:119], s[4:5] op_sel_hi:[1,0]
	v_pk_mul_f32 v[8:9], v[120:121], s[4:5] op_sel_hi:[1,0]
	v_pk_mul_f32 v[20:21], v[122:123], s[4:5] op_sel_hi:[1,0]
	v_pk_mul_f32 v[22:23], v[124:125], s[4:5] op_sel_hi:[1,0]
	v_exp_f32_e32 v6, v6
	v_exp_f32_e32 v7, v7
	v_exp_f32_e32 v8, v8
	v_exp_f32_e32 v9, v9
	v_exp_f32_e32 v20, v20
	v_exp_f32_e32 v21, v21
	v_exp_f32_e32 v22, v22
	v_exp_f32_e32 v23, v23
	v_pk_add_f32 v[6:7], v[6:7], 1.0 op_sel_hi:[1,0]
	v_pk_add_f32 v[8:9], v[8:9], 1.0 op_sel_hi:[1,0]
	v_pk_add_f32 v[20:21], v[20:21], 1.0 op_sel_hi:[1,0]
	v_pk_add_f32 v[22:23], v[22:23], 1.0 op_sel_hi:[1,0]
	v_rcp_f32_e32 v6, v6
	v_rcp_f32_e32 v7, v7
	v_rcp_f32_e32 v8, v8
	v_rcp_f32_e32 v9, v9
	v_rcp_f32_e32 v20, v20
	v_rcp_f32_e32 v21, v21
	v_rcp_f32_e32 v22, v22
	v_rcp_f32_e32 v23, v23
	v_pk_mul_f32 v[118:119], v[118:119], v[6:7]
	v_pk_mul_f32 v[120:121], v[120:121], v[8:9]
	v_pk_mul_f32 v[122:123], v[122:123], v[20:21]
	v_pk_mul_f32 v[124:125], v[124:125], v[22:23]
	v_med3_f32 v118, v118, s35, v225
	v_med3_f32 v119, v119, s35, v225
	v_med3_f32 v120, v120, s35, v225
	v_med3_f32 v121, v121, s35, v225
	v_med3_f32 v122, v122, s35, v225
	v_med3_f32 v123, v123, s35, v225
	v_med3_f32 v124, v124, s35, v225
	v_med3_f32 v125, v125, s35, v225
	v_pk_mul_f32 v[126:127], v[126:127], s[34:35] op_sel_hi:[1,0]
	v_pk_mul_f32 v[128:129], v[128:129], s[34:35] op_sel_hi:[1,0]
	v_pk_mul_f32 v[130:131], v[130:131], s[34:35] op_sel_hi:[1,0]
	v_pk_mul_f32 v[132:133], v[132:133], s[34:35] op_sel_hi:[1,0]
	v_pk_mul_f32 v[6:7], v[126:127], s[4:5] op_sel_hi:[1,0]
	v_pk_mul_f32 v[8:9], v[128:129], s[4:5] op_sel_hi:[1,0]
	v_pk_mul_f32 v[20:21], v[130:131], s[4:5] op_sel_hi:[1,0]
	v_pk_mul_f32 v[22:23], v[132:133], s[4:5] op_sel_hi:[1,0]
	v_exp_f32_e32 v6, v6
	v_exp_f32_e32 v7, v7
	v_exp_f32_e32 v8, v8
	v_exp_f32_e32 v9, v9
	v_exp_f32_e32 v20, v20
	v_exp_f32_e32 v21, v21
	v_exp_f32_e32 v22, v22
	v_exp_f32_e32 v23, v23
	v_pk_add_f32 v[6:7], v[6:7], 1.0 op_sel_hi:[1,0]
	v_pk_add_f32 v[8:9], v[8:9], 1.0 op_sel_hi:[1,0]
	v_pk_add_f32 v[20:21], v[20:21], 1.0 op_sel_hi:[1,0]
	v_pk_add_f32 v[22:23], v[22:23], 1.0 op_sel_hi:[1,0]
	v_rcp_f32_e32 v6, v6
	v_rcp_f32_e32 v7, v7
	v_rcp_f32_e32 v8, v8
	v_rcp_f32_e32 v9, v9
	v_rcp_f32_e32 v20, v20
	v_rcp_f32_e32 v21, v21
	v_rcp_f32_e32 v22, v22
	v_rcp_f32_e32 v23, v23
	v_pk_mul_f32 v[126:127], v[126:127], v[6:7]
	v_pk_mul_f32 v[128:129], v[128:129], v[8:9]
	v_pk_mul_f32 v[130:131], v[130:131], v[20:21]
	v_pk_mul_f32 v[132:133], v[132:133], v[22:23]
	v_med3_f32 v126, v126, s35, v225
	v_med3_f32 v127, v127, s35, v225
	v_med3_f32 v128, v128, s35, v225
	v_med3_f32 v129, v129, s35, v225
	v_med3_f32 v130, v130, s35, v225
	v_med3_f32 v131, v131, s35, v225
	v_med3_f32 v132, v132, s35, v225
	v_med3_f32 v133, v133, s35, v225
	v_cvt_pk_fp8_f32 v126, v126, v127
	v_cvt_pk_fp8_f32 v127, v118, v119
	v_cvt_pk_fp8_f32 v126, v128, v129 op_sel:[0,0,1]
	v_cvt_pk_fp8_f32 v127, v120, v121 op_sel:[0,0,1]
	v_cvt_pk_fp8_f32 v128, v130, v131
	v_cvt_pk_fp8_f32 v129, v122, v123
	v_cvt_pk_fp8_f32 v128, v132, v133 op_sel:[0,0,1]
	v_cvt_pk_fp8_f32 v129, v124, v125 op_sel:[0,0,1]
	v_add_co_u32_e32 v14, vcc, 0x8000, v12
	s_nop 0
	v_permlane16_swap_b32_e32 v126, v128
; DI unsigned pk4_fp8(float a, float b, float c_, float d) { int w = 0; w = __builtin_amdgcn_cvt_pk_fp8_f32(clamp8(a), clamp8(b), w, false); w = __builtin_amdgcn_cvt_pk_fp8_f32(clamp8(c_), clamp8(d), w, true); return (unsigned)w; }
; DI float sigmoidf_(float x) { return __builtin_amdgcn_rcpf(1.0f + __builtin_amdgcn_exp2f(-x * LOG2E)); }
;     DI void operator()(const f32x4 (&acc)[2][2][4][2], const Unit& u, int wr, int wc, int fr, int fq) const {
;     ...
;                     for (int m = 0; m < 4; ++m) { unsigned char* rowp = (unsigned char*)sr + (size_t)(row0 + ai * 128 + m * 16) * 1024 + (pn - 8) * 256 + wc * 32 + 8 * fq;
;                         u32x2 o[2];
; #pragma unroll
;                         for (int bj = 0; bj < 2; ++bj) { const f32x4 v0 = acc[ai][bj][m][0] * W8_INV, v1 = acc[ai][bj][m][1] * W8_INV;
;                             o[bj].x = pk4_fp8(v0[0] * sigmoidf_(v0[0]), v0[1] * sigmoidf_(v0[1]), v0[2] * sigmoidf_(v0[2]), v0[3] * sigmoidf_(v0[3]));
;                             o[bj].y = pk4_fp8(v1[0] * sigmoidf_(v1[0]), v1[1] * sigmoidf_(v1[1]), v1[2] * sigmoidf_(v1[2]), v1[3] * sigmoidf_(v1[3])); }
;                         st_pair16(rowp, 128, o[0], o[1], fq); }
	v_addc_co_u32_e32 v15, vcc, 0, v13, vcc
	v_permlane16_swap_b32_e32 v127, v129
	global_store_dwordx4 v[14:15], v[126:129], off
	v_pk_mul_f32 v[102:103], v[102:103], s[34:35] op_sel_hi:[1,0]
	v_pk_mul_f32 v[104:105], v[104:105], s[34:35] op_sel_hi:[1,0]
	v_pk_mul_f32 v[106:107], v[106:107], s[34:35] op_sel_hi:[1,0]
	v_pk_mul_f32 v[108:109], v[108:109], s[34:35] op_sel_hi:[1,0]
	v_pk_mul_f32 v[6:7], v[102:103], s[4:5] op_sel_hi:[1,0]
	v_pk_mul_f32 v[8:9], v[104:105], s[4:5] op_sel_hi:[1,0]
	v_pk_mul_f32 v[20:21], v[106:107], s[4:5] op_sel_hi:[1,0]
	v_pk_mul_f32 v[22:23], v[108:109], s[4:5] op_sel_hi:[1,0]
	v_exp_f32_e32 v6, v6
	v_exp_f32_e32 v7, v7
	v_exp_f32_e32 v8, v8
	v_exp_f32_e32 v9, v9
	v_exp_f32_e32 v20, v20
	v_exp_f32_e32 v21, v21
	v_exp_f32_e32 v22, v22
	v_exp_f32_e32 v23, v23
	v_pk_add_f32 v[6:7], v[6:7], 1.0 op_sel_hi:[1,0]
	v_pk_add_f32 v[8:9], v[8:9], 1.0 op_sel_hi:[1,0]
	v_pk_add_f32 v[20:21], v[20:21], 1.0 op_sel_hi:[1,0]
	v_pk_add_f32 v[22:23], v[22:23], 1.0 op_sel_hi:[1,0]
	v_rcp_f32_e32 v6, v6
	v_rcp_f32_e32 v7, v7
	v_rcp_f32_e32 v8, v8
	v_rcp_f32_e32 v9, v9
	v_rcp_f32_e32 v20, v20
	v_rcp_f32_e32 v21, v21
	v_rcp_f32_e32 v22, v22
	v_rcp_f32_e32 v23, v23
	v_pk_mul_f32 v[102:103], v[102:103], v[6:7]
	v_pk_mul_f32 v[104:105], v[104:105], v[8:9]
	v_pk_mul_f32 v[106:107], v[106:107], v[20:21]
	v_pk_mul_f32 v[108:109], v[108:109], v[22:23]
	v_med3_f32 v102, v102, s35, v225
	v_med3_f32 v103, v103, s35, v225
	v_med3_f32 v104, v104, s35, v225
	v_med3_f32 v105, v105, s35, v225
	v_med3_f32 v106, v106, s35, v225
	v_med3_f32 v107, v107, s35, v225
	v_med3_f32 v108, v108, s35, v225
	v_med3_f32 v109, v109, s35, v225
	v_pk_mul_f32 v[110:111], v[110:111], s[34:35] op_sel_hi:[1,0]
	v_pk_mul_f32 v[112:113], v[112:113], s[34:35] op_sel_hi:[1,0]
	v_pk_mul_f32 v[114:115], v[114:115], s[34:35] op_sel_hi:[1,0]
	v_pk_mul_f32 v[116:117], v[116:117], s[34:35] op_sel_hi:[1,0]
	v_pk_mul_f32 v[6:7], v[110:111], s[4:5] op_sel_hi:[1,0]
	v_pk_mul_f32 v[8:9], v[112:113], s[4:5] op_sel_hi:[1,0]
	v_pk_mul_f32 v[20:21], v[114:115], s[4:5] op_sel_hi:[1,0]
	v_pk_mul_f32 v[22:23], v[116:117], s[4:5] op_sel_hi:[1,0]
	v_exp_f32_e32 v6, v6
	v_exp_f32_e32 v7, v7
	v_exp_f32_e32 v8, v8
	v_exp_f32_e32 v9, v9
	v_exp_f32_e32 v20, v20
	v_exp_f32_e32 v21, v21
	v_exp_f32_e32 v22, v22
	v_exp_f32_e32 v23, v23
	v_pk_add_f32 v[6:7], v[6:7], 1.0 op_sel_hi:[1,0]
	v_pk_add_f32 v[8:9], v[8:9], 1.0 op_sel_hi:[1,0]
	v_pk_add_f32 v[20:21], v[20:21], 1.0 op_sel_hi:[1,0]
	v_pk_add_f32 v[22:23], v[22:23], 1.0 op_sel_hi:[1,0]
	v_rcp_f32_e32 v6, v6
	v_rcp_f32_e32 v7, v7
	v_rcp_f32_e32 v8, v8
	v_rcp_f32_e32 v9, v9
	v_rcp_f32_e32 v20, v20
	v_rcp_f32_e32 v21, v21
	v_rcp_f32_e32 v22, v22
	v_rcp_f32_e32 v23, v23
	v_pk_mul_f32 v[110:111], v[110:111], v[6:7]
	v_pk_mul_f32 v[112:113], v[112:113], v[8:9]
	v_pk_mul_f32 v[114:115], v[114:115], v[20:21]
	v_pk_mul_f32 v[116:117], v[116:117], v[22:23]
	v_med3_f32 v110, v110, s35, v225
	v_med3_f32 v111, v111, s35, v225
	v_med3_f32 v112, v112, s35, v225
	v_med3_f32 v113, v113, s35, v225
	v_med3_f32 v114, v114, s35, v225
	v_med3_f32 v115, v115, s35, v225
	v_med3_f32 v116, v116, s35, v225
	v_med3_f32 v117, v117, s35, v225
	v_cvt_pk_fp8_f32 v110, v110, v111
	v_cvt_pk_fp8_f32 v111, v102, v103
	v_cvt_pk_fp8_f32 v110, v112, v113 op_sel:[0,0,1]
	v_cvt_pk_fp8_f32 v111, v104, v105 op_sel:[0,0,1]
	v_cvt_pk_fp8_f32 v112, v114, v115
	v_cvt_pk_fp8_f32 v113, v106, v107
	v_cvt_pk_fp8_f32 v112, v116, v117 op_sel:[0,0,1]
	v_cvt_pk_fp8_f32 v113, v108, v109 op_sel:[0,0,1]
	v_add_co_u32_e32 v14, vcc, 0xc000, v12
	s_nop 0
	v_permlane16_swap_b32_e32 v110, v112
	v_addc_co_u32_e32 v15, vcc, 0, v13, vcc
	v_permlane16_swap_b32_e32 v111, v113
	global_store_dwordx4 v[14:15], v[110:113], off
	v_pk_mul_f32 v[86:87], v[86:87], s[34:35] op_sel_hi:[1,0]
	v_pk_mul_f32 v[88:89], v[88:89], s[34:35] op_sel_hi:[1,0]
	v_pk_mul_f32 v[90:91], v[90:91], s[34:35] op_sel_hi:[1,0]
	v_pk_mul_f32 v[92:93], v[92:93], s[34:35] op_sel_hi:[1,0]
	v_pk_mul_f32 v[6:7], v[86:87], s[4:5] op_sel_hi:[1,0]
	v_pk_mul_f32 v[8:9], v[88:89], s[4:5] op_sel_hi:[1,0]
	v_pk_mul_f32 v[20:21], v[90:91], s[4:5] op_sel_hi:[1,0]
	v_pk_mul_f32 v[22:23], v[92:93], s[4:5] op_sel_hi:[1,0]
	v_exp_f32_e32 v6, v6
	v_exp_f32_e32 v7, v7
	v_exp_f32_e32 v8, v8
	v_exp_f32_e32 v9, v9
	v_exp_f32_e32 v20, v20
	v_exp_f32_e32 v21, v21
	v_exp_f32_e32 v22, v22
	v_exp_f32_e32 v23, v23
	v_pk_add_f32 v[6:7], v[6:7], 1.0 op_sel_hi:[1,0]
	v_pk_add_f32 v[8:9], v[8:9], 1.0 op_sel_hi:[1,0]
	v_pk_add_f32 v[20:21], v[20:21], 1.0 op_sel_hi:[1,0]
	v_pk_add_f32 v[22:23], v[22:23], 1.0 op_sel_hi:[1,0]
	v_rcp_f32_e32 v6, v6
	v_rcp_f32_e32 v7, v7
	v_rcp_f32_e32 v8, v8
	v_rcp_f32_e32 v9, v9
	v_rcp_f32_e32 v20, v20
	v_rcp_f32_e32 v21, v21
	v_rcp_f32_e32 v22, v22
	v_rcp_f32_e32 v23, v23
	v_pk_mul_f32 v[86:87], v[86:87], v[6:7]
	v_pk_mul_f32 v[88:89], v[88:89], v[8:9]
	v_pk_mul_f32 v[90:91], v[90:91], v[20:21]
	v_pk_mul_f32 v[92:93], v[92:93], v[22:23]
	v_med3_f32 v86, v86, s35, v225
	v_med3_f32 v87, v87, s35, v225
	v_med3_f32 v88, v88, s35, v225
	v_med3_f32 v89, v89, s35, v225
	v_med3_f32 v90, v90, s35, v225
	v_med3_f32 v91, v91, s35, v225
	v_med3_f32 v92, v92, s35, v225
	v_med3_f32 v93, v93, s35, v225
	v_pk_mul_f32 v[94:95], v[94:95], s[34:35] op_sel_hi:[1,0]
	v_pk_mul_f32 v[96:97], v[96:97], s[34:35] op_sel_hi:[1,0]
	v_pk_mul_f32 v[98:99], v[98:99], s[34:35] op_sel_hi:[1,0]
	v_pk_mul_f32 v[100:101], v[100:101], s[34:35] op_sel_hi:[1,0]
	v_pk_mul_f32 v[6:7], v[94:95], s[4:5] op_sel_hi:[1,0]
	v_pk_mul_f32 v[8:9], v[96:97], s[4:5] op_sel_hi:[1,0]
	v_pk_mul_f32 v[20:21], v[98:99], s[4:5] op_sel_hi:[1,0]
	v_pk_mul_f32 v[22:23], v[100:101], s[4:5] op_sel_hi:[1,0]
; DI unsigned pk4_fp8(float a, float b, float c_, float d) { int w = 0; w = __builtin_amdgcn_cvt_pk_fp8_f32(clamp8(a), clamp8(b), w, false); w = __builtin_amdgcn_cvt_pk_fp8_f32(clamp8(c_), clamp8(d), w, true); return (unsigned)w; }
; DI float sigmoidf_(float x) { return __builtin_amdgcn_rcpf(1.0f + __builtin_amdgcn_exp2f(-x * LOG2E)); }
;     DI void operator()(const f32x4 (&acc)[2][2][4][2], const Unit& u, int wr, int wc, int fr, int fq) const {
;     ...
;                     for (int m = 0; m < 4; ++m) { unsigned char* rowp = (unsigned char*)sr + (size_t)(row0 + ai * 128 + m * 16) * 1024 + (pn - 8) * 256 + wc * 32 + 8 * fq;
;                         u32x2 o[2];
; #pragma unroll
;                         for (int bj = 0; bj < 2; ++bj) { const f32x4 v0 = acc[ai][bj][m][0] * W8_INV, v1 = acc[ai][bj][m][1] * W8_INV;
;                             o[bj].x = pk4_fp8(v0[0] * sigmoidf_(v0[0]), v0[1] * sigmoidf_(v0[1]), v0[2] * sigmoidf_(v0[2]), v0[3] * sigmoidf_(v0[3]));
;                             o[bj].y = pk4_fp8(v1[0] * sigmoidf_(v1[0]), v1[1] * sigmoidf_(v1[1]), v1[2] * sigmoidf_(v1[2]), v1[3] * sigmoidf_(v1[3])); }
;                         st_pair16(rowp, 128, o[0], o[1], fq); }
	v_exp_f32_e32 v6, v6
	v_exp_f32_e32 v7, v7
	v_exp_f32_e32 v8, v8
	v_exp_f32_e32 v9, v9
	v_exp_f32_e32 v20, v20
	v_exp_f32_e32 v21, v21
	v_exp_f32_e32 v22, v22
	v_exp_f32_e32 v23, v23
	v_pk_add_f32 v[6:7], v[6:7], 1.0 op_sel_hi:[1,0]
	v_pk_add_f32 v[8:9], v[8:9], 1.0 op_sel_hi:[1,0]
	v_pk_add_f32 v[20:21], v[20:21], 1.0 op_sel_hi:[1,0]
	v_pk_add_f32 v[22:23], v[22:23], 1.0 op_sel_hi:[1,0]
	v_rcp_f32_e32 v6, v6
	v_rcp_f32_e32 v7, v7
	v_rcp_f32_e32 v8, v8
	v_rcp_f32_e32 v9, v9
	v_rcp_f32_e32 v20, v20
	v_rcp_f32_e32 v21, v21
	v_rcp_f32_e32 v22, v22
	v_rcp_f32_e32 v23, v23
	v_pk_mul_f32 v[94:95], v[94:95], v[6:7]
	v_pk_mul_f32 v[96:97], v[96:97], v[8:9]
	v_pk_mul_f32 v[98:99], v[98:99], v[20:21]
	v_pk_mul_f32 v[100:101], v[100:101], v[22:23]
	v_med3_f32 v94, v94, s35, v225
	v_med3_f32 v95, v95, s35, v225
	v_med3_f32 v96, v96, s35, v225
	v_med3_f32 v97, v97, s35, v225
	v_med3_f32 v98, v98, s35, v225
	v_med3_f32 v99, v99, s35, v225
	v_med3_f32 v100, v100, s35, v225
	v_med3_f32 v101, v101, s35, v225
	v_cvt_pk_fp8_f32 v94, v94, v95
	v_cvt_pk_fp8_f32 v95, v86, v87
	v_cvt_pk_fp8_f32 v94, v96, v97 op_sel:[0,0,1]
	v_cvt_pk_fp8_f32 v95, v88, v89 op_sel:[0,0,1]
	v_cvt_pk_fp8_f32 v96, v98, v99
	v_cvt_pk_fp8_f32 v97, v90, v91
	v_cvt_pk_fp8_f32 v96, v100, v101 op_sel:[0,0,1]
	v_cvt_pk_fp8_f32 v97, v92, v93 op_sel:[0,0,1]
	v_add_co_u32_e32 v14, vcc, 0x20000, v12
	s_nop 0
	v_permlane16_swap_b32_e32 v94, v96
	v_addc_co_u32_e32 v15, vcc, 0, v13, vcc
	v_permlane16_swap_b32_e32 v95, v97
	global_store_dwordx4 v[14:15], v[94:97], off
	v_pk_mul_f32 v[70:71], v[70:71], s[34:35] op_sel_hi:[1,0]
	v_pk_mul_f32 v[72:73], v[72:73], s[34:35] op_sel_hi:[1,0]
	v_pk_mul_f32 v[74:75], v[74:75], s[34:35] op_sel_hi:[1,0]
	v_pk_mul_f32 v[76:77], v[76:77], s[34:35] op_sel_hi:[1,0]
	v_pk_mul_f32 v[6:7], v[70:71], s[4:5] op_sel_hi:[1,0]
	v_pk_mul_f32 v[8:9], v[72:73], s[4:5] op_sel_hi:[1,0]
	v_pk_mul_f32 v[20:21], v[74:75], s[4:5] op_sel_hi:[1,0]
	v_pk_mul_f32 v[22:23], v[76:77], s[4:5] op_sel_hi:[1,0]
	v_exp_f32_e32 v6, v6
	v_exp_f32_e32 v7, v7
	v_exp_f32_e32 v8, v8
	v_exp_f32_e32 v9, v9
	v_exp_f32_e32 v20, v20
	v_exp_f32_e32 v21, v21
	v_exp_f32_e32 v22, v22
	v_exp_f32_e32 v23, v23
	v_pk_add_f32 v[6:7], v[6:7], 1.0 op_sel_hi:[1,0]
	v_pk_add_f32 v[8:9], v[8:9], 1.0 op_sel_hi:[1,0]
	v_pk_add_f32 v[20:21], v[20:21], 1.0 op_sel_hi:[1,0]
	v_pk_add_f32 v[22:23], v[22:23], 1.0 op_sel_hi:[1,0]
	v_rcp_f32_e32 v6, v6
	v_rcp_f32_e32 v7, v7
	v_rcp_f32_e32 v8, v8
	v_rcp_f32_e32 v9, v9
	v_rcp_f32_e32 v20, v20
	v_rcp_f32_e32 v21, v21
	v_rcp_f32_e32 v22, v22
	v_rcp_f32_e32 v23, v23
	v_pk_mul_f32 v[70:71], v[70:71], v[6:7]
	v_pk_mul_f32 v[72:73], v[72:73], v[8:9]
	v_pk_mul_f32 v[74:75], v[74:75], v[20:21]
	v_pk_mul_f32 v[76:77], v[76:77], v[22:23]
	v_med3_f32 v70, v70, s35, v225
	v_med3_f32 v71, v71, s35, v225
	v_med3_f32 v72, v72, s35, v225
	v_med3_f32 v73, v73, s35, v225
	v_med3_f32 v74, v74, s35, v225
	v_med3_f32 v75, v75, s35, v225
	v_med3_f32 v76, v76, s35, v225
	v_med3_f32 v77, v77, s35, v225
	v_pk_mul_f32 v[78:79], v[78:79], s[34:35] op_sel_hi:[1,0]
	v_pk_mul_f32 v[80:81], v[80:81], s[34:35] op_sel_hi:[1,0]
	v_pk_mul_f32 v[82:83], v[82:83], s[34:35] op_sel_hi:[1,0]
	v_pk_mul_f32 v[84:85], v[84:85], s[34:35] op_sel_hi:[1,0]
	v_pk_mul_f32 v[6:7], v[78:79], s[4:5] op_sel_hi:[1,0]
	v_pk_mul_f32 v[8:9], v[80:81], s[4:5] op_sel_hi:[1,0]
	v_pk_mul_f32 v[20:21], v[82:83], s[4:5] op_sel_hi:[1,0]
	v_pk_mul_f32 v[22:23], v[84:85], s[4:5] op_sel_hi:[1,0]
	v_exp_f32_e32 v6, v6
	v_exp_f32_e32 v7, v7
	v_exp_f32_e32 v8, v8
	v_exp_f32_e32 v9, v9
	v_exp_f32_e32 v20, v20
	v_exp_f32_e32 v21, v21
	v_exp_f32_e32 v22, v22
	v_exp_f32_e32 v23, v23
	v_pk_add_f32 v[6:7], v[6:7], 1.0 op_sel_hi:[1,0]
	v_pk_add_f32 v[8:9], v[8:9], 1.0 op_sel_hi:[1,0]
	v_pk_add_f32 v[20:21], v[20:21], 1.0 op_sel_hi:[1,0]
	v_pk_add_f32 v[22:23], v[22:23], 1.0 op_sel_hi:[1,0]
	v_rcp_f32_e32 v6, v6
	v_rcp_f32_e32 v7, v7
	v_rcp_f32_e32 v8, v8
	v_rcp_f32_e32 v9, v9
	v_rcp_f32_e32 v20, v20
	v_rcp_f32_e32 v21, v21
	v_rcp_f32_e32 v22, v22
	v_rcp_f32_e32 v23, v23
	v_pk_mul_f32 v[78:79], v[78:79], v[6:7]
	v_pk_mul_f32 v[80:81], v[80:81], v[8:9]
	v_pk_mul_f32 v[82:83], v[82:83], v[20:21]
	v_pk_mul_f32 v[84:85], v[84:85], v[22:23]
	v_med3_f32 v78, v78, s35, v225
	v_med3_f32 v79, v79, s35, v225
	v_med3_f32 v80, v80, s35, v225
	v_med3_f32 v81, v81, s35, v225
	v_med3_f32 v82, v82, s35, v225
	v_med3_f32 v83, v83, s35, v225
	v_med3_f32 v84, v84, s35, v225
	v_med3_f32 v85, v85, s35, v225
	v_cvt_pk_fp8_f32 v78, v78, v79
	v_cvt_pk_fp8_f32 v79, v70, v71
	v_cvt_pk_fp8_f32 v78, v80, v81 op_sel:[0,0,1]
	v_cvt_pk_fp8_f32 v79, v72, v73 op_sel:[0,0,1]
	v_cvt_pk_fp8_f32 v80, v82, v83
	v_cvt_pk_fp8_f32 v81, v74, v75
	v_cvt_pk_fp8_f32 v80, v84, v85 op_sel:[0,0,1]
	v_cvt_pk_fp8_f32 v81, v76, v77 op_sel:[0,0,1]
	v_add_co_u32_e32 v14, vcc, 0x24000, v12
	s_nop 0
	v_permlane16_swap_b32_e32 v78, v80
	v_addc_co_u32_e32 v15, vcc, 0, v13, vcc
	v_permlane16_swap_b32_e32 v79, v81
	global_store_dwordx4 v[14:15], v[78:81], off
	v_pk_mul_f32 v[54:55], v[54:55], s[34:35] op_sel_hi:[1,0]
	v_pk_mul_f32 v[56:57], v[56:57], s[34:35] op_sel_hi:[1,0]
	v_pk_mul_f32 v[58:59], v[58:59], s[34:35] op_sel_hi:[1,0]
	v_pk_mul_f32 v[60:61], v[60:61], s[34:35] op_sel_hi:[1,0]
	v_pk_mul_f32 v[6:7], v[54:55], s[4:5] op_sel_hi:[1,0]
	v_pk_mul_f32 v[8:9], v[56:57], s[4:5] op_sel_hi:[1,0]
	v_pk_mul_f32 v[20:21], v[58:59], s[4:5] op_sel_hi:[1,0]
	v_pk_mul_f32 v[22:23], v[60:61], s[4:5] op_sel_hi:[1,0]
	v_exp_f32_e32 v6, v6
	v_exp_f32_e32 v7, v7
	v_exp_f32_e32 v8, v8
	v_exp_f32_e32 v9, v9
	v_exp_f32_e32 v20, v20
	v_exp_f32_e32 v21, v21
	v_exp_f32_e32 v22, v22
	v_exp_f32_e32 v23, v23
; DI unsigned pk4_fp8(float a, float b, float c_, float d) { int w = 0; w = __builtin_amdgcn_cvt_pk_fp8_f32(clamp8(a), clamp8(b), w, false); w = __builtin_amdgcn_cvt_pk_fp8_f32(clamp8(c_), clamp8(d), w, true); return (unsigned)w; }
; DI float sigmoidf_(float x) { return __builtin_amdgcn_rcpf(1.0f + __builtin_amdgcn_exp2f(-x * LOG2E)); }
;     DI void operator()(const f32x4 (&acc)[2][2][4][2], const Unit& u, int wr, int wc, int fr, int fq) const {
;     ...
;                     for (int m = 0; m < 4; ++m) { unsigned char* rowp = (unsigned char*)sr + (size_t)(row0 + ai * 128 + m * 16) * 1024 + (pn - 8) * 256 + wc * 32 + 8 * fq;
;                         u32x2 o[2];
; #pragma unroll
;                         for (int bj = 0; bj < 2; ++bj) { const f32x4 v0 = acc[ai][bj][m][0] * W8_INV, v1 = acc[ai][bj][m][1] * W8_INV;
;                             o[bj].x = pk4_fp8(v0[0] * sigmoidf_(v0[0]), v0[1] * sigmoidf_(v0[1]), v0[2] * sigmoidf_(v0[2]), v0[3] * sigmoidf_(v0[3]));
;                             o[bj].y = pk4_fp8(v1[0] * sigmoidf_(v1[0]), v1[1] * sigmoidf_(v1[1]), v1[2] * sigmoidf_(v1[2]), v1[3] * sigmoidf_(v1[3])); }
;                         st_pair16(rowp, 128, o[0], o[1], fq); }
	v_pk_add_f32 v[6:7], v[6:7], 1.0 op_sel_hi:[1,0]
	v_pk_add_f32 v[8:9], v[8:9], 1.0 op_sel_hi:[1,0]
	v_pk_add_f32 v[20:21], v[20:21], 1.0 op_sel_hi:[1,0]
	v_pk_add_f32 v[22:23], v[22:23], 1.0 op_sel_hi:[1,0]
	v_rcp_f32_e32 v6, v6
	v_rcp_f32_e32 v7, v7
	v_rcp_f32_e32 v8, v8
	v_rcp_f32_e32 v9, v9
	v_rcp_f32_e32 v20, v20
	v_rcp_f32_e32 v21, v21
	v_rcp_f32_e32 v22, v22
	v_rcp_f32_e32 v23, v23
	v_pk_mul_f32 v[54:55], v[54:55], v[6:7]
	v_pk_mul_f32 v[56:57], v[56:57], v[8:9]
	v_pk_mul_f32 v[58:59], v[58:59], v[20:21]
	v_pk_mul_f32 v[60:61], v[60:61], v[22:23]
	v_med3_f32 v54, v54, s35, v225
	v_med3_f32 v55, v55, s35, v225
	v_med3_f32 v56, v56, s35, v225
	v_med3_f32 v57, v57, s35, v225
	v_med3_f32 v58, v58, s35, v225
	v_med3_f32 v59, v59, s35, v225
	v_med3_f32 v60, v60, s35, v225
	v_med3_f32 v61, v61, s35, v225
	v_pk_mul_f32 v[62:63], v[62:63], s[34:35] op_sel_hi:[1,0]
	v_pk_mul_f32 v[64:65], v[64:65], s[34:35] op_sel_hi:[1,0]
	v_pk_mul_f32 v[66:67], v[66:67], s[34:35] op_sel_hi:[1,0]
	v_pk_mul_f32 v[68:69], v[68:69], s[34:35] op_sel_hi:[1,0]
	v_pk_mul_f32 v[6:7], v[62:63], s[4:5] op_sel_hi:[1,0]
	v_pk_mul_f32 v[8:9], v[64:65], s[4:5] op_sel_hi:[1,0]
	v_pk_mul_f32 v[20:21], v[66:67], s[4:5] op_sel_hi:[1,0]
	v_pk_mul_f32 v[22:23], v[68:69], s[4:5] op_sel_hi:[1,0]
	v_exp_f32_e32 v6, v6
	v_exp_f32_e32 v7, v7
	v_exp_f32_e32 v8, v8
	v_exp_f32_e32 v9, v9
	v_exp_f32_e32 v20, v20
	v_exp_f32_e32 v21, v21
	v_exp_f32_e32 v22, v22
	v_exp_f32_e32 v23, v23
	v_pk_add_f32 v[6:7], v[6:7], 1.0 op_sel_hi:[1,0]
	v_pk_add_f32 v[8:9], v[8:9], 1.0 op_sel_hi:[1,0]
	v_pk_add_f32 v[20:21], v[20:21], 1.0 op_sel_hi:[1,0]
	v_pk_add_f32 v[22:23], v[22:23], 1.0 op_sel_hi:[1,0]
	v_rcp_f32_e32 v6, v6
	v_rcp_f32_e32 v7, v7
	v_rcp_f32_e32 v8, v8
	v_rcp_f32_e32 v9, v9
	v_rcp_f32_e32 v20, v20
	v_rcp_f32_e32 v21, v21
	v_rcp_f32_e32 v22, v22
	v_rcp_f32_e32 v23, v23
	v_pk_mul_f32 v[62:63], v[62:63], v[6:7]
	v_pk_mul_f32 v[64:65], v[64:65], v[8:9]
	v_pk_mul_f32 v[66:67], v[66:67], v[20:21]
	v_pk_mul_f32 v[68:69], v[68:69], v[22:23]
	v_med3_f32 v62, v62, s35, v225
	v_med3_f32 v63, v63, s35, v225
	v_med3_f32 v64, v64, s35, v225
	v_med3_f32 v65, v65, s35, v225
	v_med3_f32 v66, v66, s35, v225
	v_med3_f32 v67, v67, s35, v225
	v_med3_f32 v68, v68, s35, v225
	v_med3_f32 v69, v69, s35, v225
	v_cvt_pk_fp8_f32 v62, v62, v63
	v_cvt_pk_fp8_f32 v63, v54, v55
	v_cvt_pk_fp8_f32 v62, v64, v65 op_sel:[0,0,1]
	v_cvt_pk_fp8_f32 v63, v56, v57 op_sel:[0,0,1]
	v_cvt_pk_fp8_f32 v64, v66, v67
	v_cvt_pk_fp8_f32 v65, v58, v59
	v_cvt_pk_fp8_f32 v64, v68, v69 op_sel:[0,0,1]
	v_cvt_pk_fp8_f32 v65, v60, v61 op_sel:[0,0,1]
	v_add_co_u32_e32 v14, vcc, 0x28000, v12
	s_nop 0
	v_permlane16_swap_b32_e32 v62, v64
	v_addc_co_u32_e32 v15, vcc, 0, v13, vcc
	v_permlane16_swap_b32_e32 v63, v65
	global_store_dwordx4 v[14:15], v[62:65], off
	v_pk_mul_f32 v[38:39], v[38:39], s[34:35] op_sel_hi:[1,0]
	v_pk_mul_f32 v[40:41], v[40:41], s[34:35] op_sel_hi:[1,0]
	v_pk_mul_f32 v[42:43], v[42:43], s[34:35] op_sel_hi:[1,0]
	v_pk_mul_f32 v[44:45], v[44:45], s[34:35] op_sel_hi:[1,0]
	v_pk_mul_f32 v[6:7], v[38:39], s[4:5] op_sel_hi:[1,0]
	v_pk_mul_f32 v[8:9], v[40:41], s[4:5] op_sel_hi:[1,0]
	v_pk_mul_f32 v[20:21], v[42:43], s[4:5] op_sel_hi:[1,0]
	v_pk_mul_f32 v[22:23], v[44:45], s[4:5] op_sel_hi:[1,0]
	v_exp_f32_e32 v6, v6
	v_exp_f32_e32 v7, v7
	v_exp_f32_e32 v8, v8
	v_exp_f32_e32 v9, v9
	v_exp_f32_e32 v20, v20
	v_exp_f32_e32 v21, v21
	v_exp_f32_e32 v22, v22
	v_exp_f32_e32 v23, v23
	v_pk_add_f32 v[6:7], v[6:7], 1.0 op_sel_hi:[1,0]
	v_pk_add_f32 v[8:9], v[8:9], 1.0 op_sel_hi:[1,0]
	v_pk_add_f32 v[20:21], v[20:21], 1.0 op_sel_hi:[1,0]
	v_pk_add_f32 v[22:23], v[22:23], 1.0 op_sel_hi:[1,0]
	v_rcp_f32_e32 v6, v6
	v_rcp_f32_e32 v7, v7
	v_rcp_f32_e32 v8, v8
	v_rcp_f32_e32 v9, v9
	v_rcp_f32_e32 v20, v20
	v_rcp_f32_e32 v21, v21
	v_rcp_f32_e32 v22, v22
	v_rcp_f32_e32 v23, v23
	v_pk_mul_f32 v[38:39], v[38:39], v[6:7]
	v_pk_mul_f32 v[40:41], v[40:41], v[8:9]
	v_pk_mul_f32 v[42:43], v[42:43], v[20:21]
	v_pk_mul_f32 v[44:45], v[44:45], v[22:23]
	v_med3_f32 v38, v38, s35, v225
	v_med3_f32 v39, v39, s35, v225
	v_med3_f32 v40, v40, s35, v225
	v_med3_f32 v41, v41, s35, v225
	v_med3_f32 v42, v42, s35, v225
	v_med3_f32 v43, v43, s35, v225
	v_med3_f32 v44, v44, s35, v225
	v_med3_f32 v45, v45, s35, v225
	v_pk_mul_f32 v[46:47], v[46:47], s[34:35] op_sel_hi:[1,0]
	v_pk_mul_f32 v[48:49], v[48:49], s[34:35] op_sel_hi:[1,0]
	v_pk_mul_f32 v[50:51], v[50:51], s[34:35] op_sel_hi:[1,0]
	v_pk_mul_f32 v[52:53], v[52:53], s[34:35] op_sel_hi:[1,0]
	v_pk_mul_f32 v[6:7], v[46:47], s[4:5] op_sel_hi:[1,0]
	v_pk_mul_f32 v[8:9], v[48:49], s[4:5] op_sel_hi:[1,0]
	v_pk_mul_f32 v[20:21], v[50:51], s[4:5] op_sel_hi:[1,0]
	v_pk_mul_f32 v[22:23], v[52:53], s[4:5] op_sel_hi:[1,0]
	v_exp_f32_e32 v6, v6
	v_exp_f32_e32 v7, v7
	v_exp_f32_e32 v8, v8
	v_exp_f32_e32 v9, v9
	v_exp_f32_e32 v20, v20
	v_exp_f32_e32 v21, v21
	v_exp_f32_e32 v22, v22
	v_exp_f32_e32 v23, v23
	v_pk_add_f32 v[6:7], v[6:7], 1.0 op_sel_hi:[1,0]
	v_pk_add_f32 v[8:9], v[8:9], 1.0 op_sel_hi:[1,0]
	v_pk_add_f32 v[20:21], v[20:21], 1.0 op_sel_hi:[1,0]
	v_pk_add_f32 v[22:23], v[22:23], 1.0 op_sel_hi:[1,0]
	v_rcp_f32_e32 v6, v6
	v_rcp_f32_e32 v7, v7
	v_rcp_f32_e32 v8, v8
	v_rcp_f32_e32 v9, v9
	v_rcp_f32_e32 v20, v20
	v_rcp_f32_e32 v21, v21
	v_rcp_f32_e32 v22, v22
	v_rcp_f32_e32 v23, v23
	v_pk_mul_f32 v[46:47], v[46:47], v[6:7]
	v_pk_mul_f32 v[48:49], v[48:49], v[8:9]
	v_pk_mul_f32 v[50:51], v[50:51], v[20:21]
	v_pk_mul_f32 v[52:53], v[52:53], v[22:23]
	v_med3_f32 v46, v46, s35, v225
	v_med3_f32 v47, v47, s35, v225
	v_med3_f32 v48, v48, s35, v225
	v_med3_f32 v49, v49, s35, v225
	v_med3_f32 v50, v50, s35, v225
	v_med3_f32 v51, v51, s35, v225
	v_med3_f32 v52, v52, s35, v225
	v_med3_f32 v53, v53, s35, v225
	v_cvt_pk_fp8_f32 v46, v46, v47
	v_cvt_pk_fp8_f32 v47, v38, v39
	v_cvt_pk_fp8_f32 v46, v48, v49 op_sel:[0,0,1]
	v_cvt_pk_fp8_f32 v47, v40, v41 op_sel:[0,0,1]
	v_cvt_pk_fp8_f32 v48, v50, v51
	v_cvt_pk_fp8_f32 v49, v42, v43
	v_cvt_pk_fp8_f32 v48, v52, v53 op_sel:[0,0,1]
	v_cvt_pk_fp8_f32 v49, v44, v45 op_sel:[0,0,1]
	v_add_co_u32_e32 v14, vcc, 0x2c000, v12
	s_nop 0
	v_permlane16_swap_b32_e32 v46, v48
	v_addc_co_u32_e32 v15, vcc, 0, v13, vcc
	v_permlane16_swap_b32_e32 v47, v49
	global_store_dwordx4 v[14:15], v[46:49], off
